# removed 7 grid barriers between independent phases (conv->ffn1 norm, ffn2 down->next colmax) and the final one; scan v3
# speedup vs baseline: 1.0185x; 1.0017x over previous
; __device__ __forceinline__ unsigned xb_ld(unsigned* p)              { return __hip_atomic_load(p, __ATOMIC_RELAXED, __HIP_MEMORY_SCOPE_AGENT); }
; __device__ __forceinline__ unsigned xb_add(unsigned* p, unsigned v) { return __hip_atomic_fetch_add(p, v, __ATOMIC_RELAXED, __HIP_MEMORY_SCOPE_AGENT); }
; #define XB_SPIN(cond, bar) do { unsigned _sp = 0; while (cond) { __builtin_amdgcn_s_sleep(1); \
;     if ((++_sp & 255u) == 0u) { if (xb_ld(&(bar)[XB_TMO])) break; if (_sp > XB_SPIN_CAP) { atomicAdd(&(bar)[XB_TMO], 1u); break; } } } } while (0)
; __device__ __forceinline__ void xcd_barrier(const XcdBarrier& b) {
;     asm volatile("s_waitcnt vmcnt(0)" ::: "memory");
;     __syncthreads();
;     if (threadIdx.x == 0) {
;         unsigned* bar = b.bar;
;         __builtin_amdgcn_s_waitcnt(0);
;         unsigned nloc = b.st[0], nx = b.st[1];
;         if (nloc == 0u) { xcd_barrier_complete(bar, b.x, nloc, nx); b.st[0] = nloc; b.st[1] = nx; }
;         const unsigned old = xb_add(&bar[XB_XSUB(b.x)], 1u);
;         const unsigned gen = old / nloc;
;         if (old + 1u == (gen + 1u) * nloc) {
;             __builtin_amdgcn_fence(__ATOMIC_RELEASE, "agent");
;             asm volatile("s_waitcnt vmcnt(0)" ::: "memory");
;             const unsigned og = xb_add(&bar[XB_TOP], 1u);
;             const unsigned tg = og / nx;
;             if (og + 1u == (tg + 1u) * nx) xb_add(&bar[XB_TOPGEN], 1u);
;             else XB_SPIN(xb_ld(&bar[XB_TOPGEN]) == tg, bar);
;             __builtin_amdgcn_fence(__ATOMIC_ACQUIRE, "agent");
;             xb_add(&bar[XB_XGEN(b.x)], 1u);
;             asm volatile("s_waitcnt vmcnt(0)" ::: "memory");
;         } else {
;             XB_SPIN(xb_ld(&bar[XB_XGEN(b.x)]) == gen, bar);
;             __builtin_amdgcn_fence(__ATOMIC_ACQUIRE, "agent");
;             asm volatile("s_waitcnt vmcnt(0)" ::: "memory");
;         }
;     }
;     __syncthreads();
; }
.LBB0_101:
	v_readlane_b32 s7, v247, 8
	s_cmp_lt_i32 s7, 3
	s_branch .LBB0_147
	v_readlane_b32 s34, v247, 2
	v_readlane_b32 s35, v247, 3
	s_waitcnt vmcnt(0)
	s_waitcnt lgkmcnt(0)
	s_barrier
	s_mov_b64 s[30:31], exec
	v_readlane_b32 s0, v247, 5
	v_readlane_b32 s1, v247, 6
	s_and_b64 s[0:1], s[30:31], s[0:1]
	s_mov_b64 exec, s[0:1]
	s_cbranch_execz .LBB0_146
	s_add_i32 s0, 0, 0x20160
	v_mov_b32_e32 v1, s0
	s_waitcnt vmcnt(0) expcnt(0) lgkmcnt(0)
	ds_read_b32 v4, v1
	s_add_i32 s0, 0, 0x20164
	v_mov_b32_e32 v1, s0
	ds_read_b32 v2, v1
	s_waitcnt lgkmcnt(1)
	v_cmp_ne_u32_e32 vcc, 0, v4
	s_cbranch_vccnz .LBB0_117
	s_load_dwordx2 s[0:1], s[2:3], 0x4
	s_add_u32 s2, s34, 0x1000
	s_addc_u32 s3, s35, 0
	s_add_u32 s4, s34, 0x1100
	s_addc_u32 s5, s35, 0
	s_add_u32 s6, s34, 0x1200
	s_addc_u32 s7, s35, 0
	s_add_u32 s8, s34, 0x1300
	s_waitcnt lgkmcnt(0)
	s_mul_i32 s18, s0, s18
	s_addc_u32 s9, s35, 0
	s_mul_i32 s18, s18, s1
	s_mov_b32 s19, 1
	s_mov_b64 s[0:1], 0
	v_mov_b64_e32 v[2:3], s[34:35]
	v_mov_b64_e32 v[4:5], s[2:3]
	v_mov_b64_e32 v[6:7], s[4:5]
	v_mov_b64_e32 v[8:9], s[6:7]
	v_mov_b64_e32 v[10:11], s[8:9]
	s_branch .LBB0_107

; __device__ __forceinline__ unsigned xb_ld(unsigned* p)              { return __hip_atomic_load(p, __ATOMIC_RELAXED, __HIP_MEMORY_SCOPE_AGENT); }
; __device__ __forceinline__ unsigned xb_add(unsigned* p, unsigned v) { return __hip_atomic_fetch_add(p, v, __ATOMIC_RELAXED, __HIP_MEMORY_SCOPE_AGENT); }
; #define XB_SPIN(cond, bar) do { unsigned _sp = 0; while (cond) { __builtin_amdgcn_s_sleep(1); \
;     if ((++_sp & 255u) == 0u) { if (xb_ld(&(bar)[XB_TMO])) break; if (_sp > XB_SPIN_CAP) { atomicAdd(&(bar)[XB_TMO], 1u); break; } } } } while (0)
; __device__ __forceinline__ void xcd_barrier(const XcdBarrier& b) {
;     asm volatile("s_waitcnt vmcnt(0)" ::: "memory");
;     __syncthreads();
;     if (threadIdx.x == 0) {
;         unsigned* bar = b.bar;
;         __builtin_amdgcn_s_waitcnt(0);
;         unsigned nloc = b.st[0], nx = b.st[1];
;         if (nloc == 0u) { xcd_barrier_complete(bar, b.x, nloc, nx); b.st[0] = nloc; b.st[1] = nx; }
;         const unsigned old = xb_add(&bar[XB_XSUB(b.x)], 1u);
;         const unsigned gen = old / nloc;
;         if (old + 1u == (gen + 1u) * nloc) {
;             __builtin_amdgcn_fence(__ATOMIC_RELEASE, "agent");
;             asm volatile("s_waitcnt vmcnt(0)" ::: "memory");
;             const unsigned og = xb_add(&bar[XB_TOP], 1u);
;             const unsigned tg = og / nx;
;             if (og + 1u == (tg + 1u) * nx) xb_add(&bar[XB_TOPGEN], 1u);
;             else XB_SPIN(xb_ld(&bar[XB_TOPGEN]) == tg, bar);
;             __builtin_amdgcn_fence(__ATOMIC_ACQUIRE, "agent");
;             xb_add(&bar[XB_XGEN(b.x)], 1u);
;             asm volatile("s_waitcnt vmcnt(0)" ::: "memory");
;         } else {
;             XB_SPIN(xb_ld(&bar[XB_XGEN(b.x)]) == gen, bar);
;             __builtin_amdgcn_fence(__ATOMIC_ACQUIRE, "agent");
;             asm volatile("s_waitcnt vmcnt(0)" ::: "memory");
;         }
;     }
;     __syncthreads();
; }
.LBB0_930:
	v_readlane_b32 s7, v247, 8
	s_cmp_lt_i32 s7, 14
	s_branch .LBB0_976
	v_readlane_b32 s34, v247, 2
	v_readlane_b32 s35, v247, 3
	s_waitcnt vmcnt(0)
	s_waitcnt vmcnt(0)
	s_barrier
	s_mov_b64 s[30:31], exec
	v_readlane_b32 s0, v247, 5
	v_readlane_b32 s1, v247, 6
	s_and_b64 s[0:1], s[30:31], s[0:1]
	s_mov_b64 exec, s[0:1]
	s_cbranch_execz .LBB0_975
	s_add_i32 s0, 0, 0x20160
	v_mov_b32_e32 v1, s0
	s_waitcnt vmcnt(0) expcnt(0) lgkmcnt(0)
	ds_read_b32 v4, v1
	s_add_i32 s0, 0, 0x20164
	v_mov_b32_e32 v1, s0
	ds_read_b32 v2, v1
	s_waitcnt lgkmcnt(1)
	v_cmp_ne_u32_e32 vcc, 0, v4
	s_cbranch_vccnz .LBB0_946
	s_add_u32 s2, s34, 0x1000
	s_addc_u32 s3, s35, 0
	s_load_dwordx2 s[0:1], s[4:5], 0x4
	s_add_u32 s4, s34, 0x1100
	s_addc_u32 s5, s35, 0
	s_add_u32 s6, s34, 0x1200
	s_addc_u32 s7, s35, 0
	s_add_u32 s8, s34, 0x1300
	s_waitcnt lgkmcnt(0)
	s_mul_i32 s18, s0, s33
	s_addc_u32 s9, s35, 0
	s_mul_i32 s18, s18, s1
	s_mov_b32 s19, 1
	s_mov_b64 s[0:1], 0
	v_mov_b64_e32 v[2:3], s[34:35]
	v_mov_b64_e32 v[4:5], s[2:3]
	v_mov_b64_e32 v[6:7], s[4:5]
	v_mov_b64_e32 v[8:9], s[6:7]
	v_mov_b64_e32 v[10:11], s[8:9]
	s_branch .LBB0_936

; __device__ __forceinline__ unsigned xb_ld(unsigned* p)              { return __hip_atomic_load(p, __ATOMIC_RELAXED, __HIP_MEMORY_SCOPE_AGENT); }
; __device__ __forceinline__ unsigned xb_add(unsigned* p, unsigned v) { return __hip_atomic_fetch_add(p, v, __ATOMIC_RELAXED, __HIP_MEMORY_SCOPE_AGENT); }
; #define XB_SPIN(cond, bar) do { unsigned _sp = 0; while (cond) { __builtin_amdgcn_s_sleep(1); \
;     if ((++_sp & 255u) == 0u) { if (xb_ld(&(bar)[XB_TMO])) break; if (_sp > XB_SPIN_CAP) { atomicAdd(&(bar)[XB_TMO], 1u); break; } } } } while (0)
; __device__ __forceinline__ void xcd_barrier(const XcdBarrier& b) {
;     asm volatile("s_waitcnt vmcnt(0)" ::: "memory");
;     __syncthreads();
;     if (threadIdx.x == 0) {
;         unsigned* bar = b.bar;
;         __builtin_amdgcn_s_waitcnt(0);
;         unsigned nloc = b.st[0], nx = b.st[1];
;         if (nloc == 0u) { xcd_barrier_complete(bar, b.x, nloc, nx); b.st[0] = nloc; b.st[1] = nx; }
;         const unsigned old = xb_add(&bar[XB_XSUB(b.x)], 1u);
;         const unsigned gen = old / nloc;
;         if (old + 1u == (gen + 1u) * nloc) {
;             __builtin_amdgcn_fence(__ATOMIC_RELEASE, "agent");
;             asm volatile("s_waitcnt vmcnt(0)" ::: "memory");
;             const unsigned og = xb_add(&bar[XB_TOP], 1u);
;             const unsigned tg = og / nx;
;             if (og + 1u == (tg + 1u) * nx) xb_add(&bar[XB_TOPGEN], 1u);
;             else XB_SPIN(xb_ld(&bar[XB_TOPGEN]) == tg, bar);
;             __builtin_amdgcn_fence(__ATOMIC_ACQUIRE, "agent");
;             xb_add(&bar[XB_XGEN(b.x)], 1u);
;             asm volatile("s_waitcnt vmcnt(0)" ::: "memory");
;         } else {
;             XB_SPIN(xb_ld(&bar[XB_XGEN(b.x)]) == gen, bar);
;             __builtin_amdgcn_fence(__ATOMIC_ACQUIRE, "agent");
;             asm volatile("s_waitcnt vmcnt(0)" ::: "memory");
;         }
;     }
;     __syncthreads();
; }
.LBB0_1074:
	v_readlane_b32 s7, v247, 8
	s_cmp_lt_i32 s7, 16
	s_branch .LBB0_1120
	v_readlane_b32 s34, v247, 2
	v_readlane_b32 s35, v247, 3
	s_waitcnt vmcnt(0)
	s_barrier
	s_mov_b64 s[30:31], exec
	v_readlane_b32 s0, v247, 5
	v_readlane_b32 s1, v247, 6
	s_and_b64 s[0:1], s[30:31], s[0:1]
	s_mov_b64 exec, s[0:1]
	s_cbranch_execz .LBB0_1119
	s_add_i32 s0, 0, 0x20160
	v_mov_b32_e32 v1, s0
	s_waitcnt vmcnt(0) expcnt(0) lgkmcnt(0)
	ds_read_b32 v4, v1
	s_add_i32 s0, 0, 0x20164
	v_mov_b32_e32 v1, s0
	ds_read_b32 v2, v1
	s_waitcnt lgkmcnt(1)
	v_cmp_ne_u32_e32 vcc, 0, v4
	s_cbranch_vccnz .LBB0_1090
	s_load_dwordx2 s[0:1], s[2:3], 0x4
	s_add_u32 s2, s34, 0x1000
	s_addc_u32 s3, s35, 0
	s_add_u32 s4, s34, 0x1100
	s_addc_u32 s5, s35, 0
	s_add_u32 s6, s34, 0x1200
	s_addc_u32 s7, s35, 0
	s_add_u32 s8, s34, 0x1300
	s_waitcnt lgkmcnt(0)
	s_mul_i32 s18, s0, s16
	s_addc_u32 s9, s35, 0
	s_mul_i32 s18, s18, s1
	s_mov_b32 s19, 1
	s_mov_b64 s[0:1], 0
	v_mov_b64_e32 v[2:3], s[34:35]
	v_mov_b64_e32 v[4:5], s[2:3]
	v_mov_b64_e32 v[6:7], s[4:5]
	v_mov_b64_e32 v[8:9], s[6:7]
	v_mov_b64_e32 v[10:11], s[8:9]
	s_branch .LBB0_1080

; __device__ __forceinline__ unsigned xb_ld(unsigned* p)              { return __hip_atomic_load(p, __ATOMIC_RELAXED, __HIP_MEMORY_SCOPE_AGENT); }
; __device__ __forceinline__ unsigned xb_add(unsigned* p, unsigned v) { return __hip_atomic_fetch_add(p, v, __ATOMIC_RELAXED, __HIP_MEMORY_SCOPE_AGENT); }
; #define XB_SPIN(cond, bar) do { unsigned _sp = 0; while (cond) { __builtin_amdgcn_s_sleep(1); \
;     if ((++_sp & 255u) == 0u) { if (xb_ld(&(bar)[XB_TMO])) break; if (_sp > XB_SPIN_CAP) { atomicAdd(&(bar)[XB_TMO], 1u); break; } } } } while (0)
; __device__ __forceinline__ void xcd_barrier(const XcdBarrier& b) {
;     asm volatile("s_waitcnt vmcnt(0)" ::: "memory");
;     __syncthreads();
;     if (threadIdx.x == 0) {
;         unsigned* bar = b.bar;
;         __builtin_amdgcn_s_waitcnt(0);
;         unsigned nloc = b.st[0], nx = b.st[1];
;         if (nloc == 0u) { xcd_barrier_complete(bar, b.x, nloc, nx); b.st[0] = nloc; b.st[1] = nx; }
;         const unsigned old = xb_add(&bar[XB_XSUB(b.x)], 1u);
;         const unsigned gen = old / nloc;
;         if (old + 1u == (gen + 1u) * nloc) {
;             __builtin_amdgcn_fence(__ATOMIC_RELEASE, "agent");
;             asm volatile("s_waitcnt vmcnt(0)" ::: "memory");
;             const unsigned og = xb_add(&bar[XB_TOP], 1u);
;             const unsigned tg = og / nx;
;             if (og + 1u == (tg + 1u) * nx) xb_add(&bar[XB_TOPGEN], 1u);
;             else XB_SPIN(xb_ld(&bar[XB_TOPGEN]) == tg, bar);
;             __builtin_amdgcn_fence(__ATOMIC_ACQUIRE, "agent");
;             xb_add(&bar[XB_XGEN(b.x)], 1u);
;             asm volatile("s_waitcnt vmcnt(0)" ::: "memory");
;         } else {
;             XB_SPIN(xb_ld(&bar[XB_XGEN(b.x)]) == gen, bar);
;             __builtin_amdgcn_fence(__ATOMIC_ACQUIRE, "agent");
;             asm volatile("s_waitcnt vmcnt(0)" ::: "memory");
;         }
;     }
;     __syncthreads();
; }
.LBB0_1762:
	v_readlane_b32 s7, v247, 8
	s_cmp_lt_i32 s7, 26
	s_branch .LBB0_1808
	v_readlane_b32 s34, v247, 2
	v_readlane_b32 s35, v247, 3
	s_waitcnt vmcnt(0)
	s_waitcnt vmcnt(0)
	s_barrier
	s_mov_b64 s[30:31], exec
	v_readlane_b32 s0, v247, 5
	v_readlane_b32 s1, v247, 6
	s_and_b64 s[0:1], s[30:31], s[0:1]
	s_mov_b64 exec, s[0:1]
	s_cbranch_execz .LBB0_1807
	s_add_i32 s0, 0, 0x20160
	v_mov_b32_e32 v1, s0
	s_waitcnt vmcnt(0) expcnt(0) lgkmcnt(0)
	ds_read_b32 v4, v1
	s_add_i32 s0, 0, 0x20164
	v_mov_b32_e32 v1, s0
	ds_read_b32 v2, v1
	s_waitcnt lgkmcnt(1)
	v_cmp_ne_u32_e32 vcc, 0, v4
	s_cbranch_vccnz .LBB0_1778
	s_add_u32 s2, s34, 0x1000
	s_addc_u32 s3, s35, 0
	s_load_dwordx2 s[0:1], s[4:5], 0x4
	s_add_u32 s4, s34, 0x1100
	s_addc_u32 s5, s35, 0
	s_add_u32 s6, s34, 0x1200
	s_addc_u32 s7, s35, 0
	s_add_u32 s8, s34, 0x1300
	s_waitcnt lgkmcnt(0)
	s_mul_i32 s18, s0, s33
	s_addc_u32 s9, s35, 0
	s_mul_i32 s18, s18, s1
	s_mov_b32 s19, 1
	s_mov_b64 s[0:1], 0
	v_mov_b64_e32 v[2:3], s[34:35]
	v_mov_b64_e32 v[4:5], s[2:3]
	v_mov_b64_e32 v[6:7], s[4:5]
	v_mov_b64_e32 v[8:9], s[6:7]
	v_mov_b64_e32 v[10:11], s[8:9]
	s_branch .LBB0_1768

; __device__ __forceinline__ unsigned xb_ld(unsigned* p)              { return __hip_atomic_load(p, __ATOMIC_RELAXED, __HIP_MEMORY_SCOPE_AGENT); }
; __device__ __forceinline__ unsigned xb_add(unsigned* p, unsigned v) { return __hip_atomic_fetch_add(p, v, __ATOMIC_RELAXED, __HIP_MEMORY_SCOPE_AGENT); }
; #define XB_SPIN(cond, bar) do { unsigned _sp = 0; while (cond) { __builtin_amdgcn_s_sleep(1); \
;     if ((++_sp & 255u) == 0u) { if (xb_ld(&(bar)[XB_TMO])) break; if (_sp > XB_SPIN_CAP) { atomicAdd(&(bar)[XB_TMO], 1u); break; } } } } while (0)
; __device__ __forceinline__ void xcd_barrier(const XcdBarrier& b) {
;     asm volatile("s_waitcnt vmcnt(0)" ::: "memory");
;     __syncthreads();
;     if (threadIdx.x == 0) {
;         unsigned* bar = b.bar;
;         __builtin_amdgcn_s_waitcnt(0);
;         unsigned nloc = b.st[0], nx = b.st[1];
;         if (nloc == 0u) { xcd_barrier_complete(bar, b.x, nloc, nx); b.st[0] = nloc; b.st[1] = nx; }
;         const unsigned old = xb_add(&bar[XB_XSUB(b.x)], 1u);
;         const unsigned gen = old / nloc;
;         if (old + 1u == (gen + 1u) * nloc) {
;             __builtin_amdgcn_fence(__ATOMIC_RELEASE, "agent");
;             asm volatile("s_waitcnt vmcnt(0)" ::: "memory");
;             const unsigned og = xb_add(&bar[XB_TOP], 1u);
;             const unsigned tg = og / nx;
;             if (og + 1u == (tg + 1u) * nx) xb_add(&bar[XB_TOPGEN], 1u);
;             else XB_SPIN(xb_ld(&bar[XB_TOPGEN]) == tg, bar);
;             __builtin_amdgcn_fence(__ATOMIC_ACQUIRE, "agent");
;             xb_add(&bar[XB_XGEN(b.x)], 1u);
;             asm volatile("s_waitcnt vmcnt(0)" ::: "memory");
;         } else {
;             XB_SPIN(xb_ld(&bar[XB_XGEN(b.x)]) == gen, bar);
;             __builtin_amdgcn_fence(__ATOMIC_ACQUIRE, "agent");
;             asm volatile("s_waitcnt vmcnt(0)" ::: "memory");
;         }
;     }
;     __syncthreads();
; }
.LBB0_1928:
	v_readlane_b32 s7, v247, 8
	s_cmp_lt_i32 s7, 28
	s_branch .LBB0_1974
	v_readlane_b32 s34, v247, 2
	v_readlane_b32 s35, v247, 3
	s_waitcnt vmcnt(0)
	s_barrier
	s_mov_b64 s[30:31], exec
	v_readlane_b32 s0, v247, 5
	v_readlane_b32 s1, v247, 6
	s_and_b64 s[0:1], s[30:31], s[0:1]
	s_mov_b64 exec, s[0:1]
	s_cbranch_execz .LBB0_1973
	s_add_i32 s0, 0, 0x20160
	v_mov_b32_e32 v1, s0
	s_waitcnt vmcnt(0) expcnt(0) lgkmcnt(0)
	ds_read_b32 v4, v1
	s_add_i32 s0, 0, 0x20164
	v_mov_b32_e32 v1, s0
	ds_read_b32 v2, v1
	s_waitcnt lgkmcnt(1)
	v_cmp_ne_u32_e32 vcc, 0, v4
	s_cbranch_vccnz .LBB0_1944
	s_add_u32 s2, s34, 0x1000
	s_addc_u32 s3, s35, 0
	s_load_dwordx2 s[0:1], s[4:5], 0x4
	s_add_u32 s4, s34, 0x1100
	s_addc_u32 s5, s35, 0
	s_add_u32 s6, s34, 0x1200
	s_addc_u32 s7, s35, 0
	s_add_u32 s8, s34, 0x1300
	s_waitcnt lgkmcnt(0)
	s_mul_i32 s18, s0, s20
	s_addc_u32 s9, s35, 0
	s_mul_i32 s18, s18, s1
	s_mov_b32 s19, 1
	s_mov_b64 s[0:1], 0
	v_mov_b64_e32 v[2:3], s[34:35]
	v_mov_b64_e32 v[4:5], s[2:3]
	v_mov_b64_e32 v[6:7], s[4:5]
	v_mov_b64_e32 v[8:9], s[6:7]
	v_mov_b64_e32 v[10:11], s[8:9]
	s_branch .LBB0_1934

; #define LAS __attribute__((address_space(3)))
; template <class AT_>
; __device__ __forceinline__ void rwkv_scan_phase(const AT_& a, Frame& F, int j) {
;     ...
;                     auto ld = [&](int t) { RwOps o; const LAS float* p = ob + t * 64 + 8 * kg;
;                         o.a0 = *(const LAS f32x4*)p; o.a1 = *(const LAS f32x4*)(p + 4); p += RW_T * 64; o.r0 = *(const LAS f32x4*)p; o.r1 = *(const LAS f32x4*)(p + 4); p += RW_T * 64;
;                         o.w0 = *(const LAS f32x4*)p; o.w1 = *(const LAS f32x4*)(p + 4); p += RW_T * 64; o.b0 = *(const LAS f32x4*)p; o.b1 = *(const LAS f32x4*)(p + 4); p += RW_T * 64;
;                         o.k0 = *(const LAS f32x4*)p; o.k1 = *(const LAS f32x4*)(p + 4);
;                         o.v = *(const LAS f32x2*)(ob + 5 * RW_T * 64 + t * 64 + v0); o.sc = *(const LAS f32x2*)(ob + 6 * RW_T * 64 + t * 4); return o; };
;                     auto step = [&](const RwOps& cur, int t) {
;                         const f32x2 a01 = {cur.a0.x, cur.a0.y}, a23 = {cur.a0.z, cur.a0.w}, a45 = {cur.a1.x, cur.a1.y}, a67 = {cur.a1.z, cur.a1.w};
;                         const f32x2 r01 = {cur.r0.x, cur.r0.y}, r23 = {cur.r0.z, cur.r0.w}, r45 = {cur.r1.x, cur.r1.y}, r67 = {cur.r1.z, cur.r1.w};
;                         f32x2 sA0 = S0[0] * a01, sA1 = S1[0] * a01, sY0 = S0[0] * r01, sY1 = S1[0] * r01;
;                         sA0 = S0[1] * a23 + sA0; sA1 = S1[1] * a23 + sA1; sY0 = S0[1] * r23 + sY0; sY1 = S1[1] * r23 + sY1;
;                         sA0 = S0[2] * a45 + sA0; sA1 = S1[2] * a45 + sA1; sY0 = S0[2] * r45 + sY0; sY1 = S1[2] * r45 + sY1;
;                         sA0 = S0[3] * a67 + sA0; sA1 = S1[3] * a67 + sA1; sY0 = S0[3] * r67 + sY0; sY1 = S1[3] * r67 + sY1;
;                         const float sa0 = row8_allsum(sA0.x + sA0.y), sa1 = row8_allsum(sA1.x + sA1.y), yy0 = row8_allsum(sY0.x + sY0.y), yy1 = row8_allsum(sY1.x + sY1.y);
;                         if (kg == 0) { f32x2 yo; yo.x = yy0 + sa0 * cur.sc.x + cur.v.x * cur.sc.y; yo.y = yy1 + sa1 * cur.sc.x + cur.v.y * cur.sc.y; *(LAS f32x2*)(Yb + t * 64 + v0) = yo; }
;                         const f32x2 w01 = {cur.w0.x, cur.w0.y}, w23 = {cur.w0.z, cur.w0.w}, w45 = {cur.w1.x, cur.w1.y}, w67 = {cur.w1.z, cur.w1.w};
;                         const f32x2 b01 = {cur.b0.x, cur.b0.y}, b23 = {cur.b0.z, cur.b0.w}, b45 = {cur.b1.x, cur.b1.y}, b67 = {cur.b1.z, cur.b1.w};
.LBB0_3512:
	s_and_b64 vcc, exec, s[42:43]
	s_cbranch_vccz .LBB0_3487
	s_cmp_lt_i32 s90, 0
	s_cselect_b64 s[42:43], -1, 0
	s_cmpk_eq_i32 s90, 0x80
	s_cselect_b64 s[44:45], -1, 0
	s_or_b64 s[42:43], s[42:43], s[44:45]
	s_and_b64 vcc, exec, s[42:43]
	s_cbranch_vccnz .LBB0_3487
	s_and_b32 s98, s90, 1
	s_mul_i32 s99, s98, 0xc200
	s_add_i32 s99, s99, s53
	v_add_u32_e32 v50, s99, v166
	v_add_u32_e32 v51, s99, v167
	v_add_u32_e32 v51, 40960, v51
	v_mov_b32_e32 v52, s99
	v_add_u32_e32 v52, 49152, v52
	s_lshl_b32 s98, s98, 13
	s_add_i32 s98, s98, s53
	s_add_i32 s98, s98, 0x18400
	v_add_u32_e32 v53, s98, v167
	ds_read_b128 v[168:171], v50 offset:0
	ds_read_b128 v[172:175], v50 offset:16
	ds_read_b128 v[176:179], v50 offset:8192
	ds_read_b128 v[180:183], v50 offset:8208
	ds_read_b128 v[184:187], v50 offset:16384
	ds_read_b128 v[188:191], v50 offset:16400
	ds_read_b128 v[192:195], v50 offset:24576
	ds_read_b128 v[196:199], v50 offset:24592
	ds_read_b128 v[200:203], v50 offset:32768
	ds_read_b128 v[204:207], v50 offset:32784
	ds_read2_b64 v[212:215], v51 offset0:0 offset1:32
	ds_read2_b64 v[216:219], v52 offset0:0 offset1:2
	v_add_u32_e32 v51, 512, v51
	v_add_u32_e32 v52, 32, v52
	s_mov_b32 s98, 4
.Lscan_a_loop:
	s_waitcnt lgkmcnt(0)
	ds_read_b128 v[2:5], v50 offset:256
	ds_read_b128 v[6:9], v50 offset:272
	ds_read_b128 v[10:13], v50 offset:8448
	ds_read_b128 v[14:17], v50 offset:8464
	ds_read_b128 v[18:21], v50 offset:16640
	ds_read_b128 v[22:25], v50 offset:16656
	ds_read_b128 v[26:29], v50 offset:24832
	ds_read_b128 v[30:33], v50 offset:24848
	ds_read_b128 v[34:37], v50 offset:33024
	ds_read_b128 v[38:41], v50 offset:33040
	ds_read2_b64 v[220:223], v51 offset0:0 offset1:32
	ds_read2_b64 v[224:227], v52 offset0:0 offset1:2
	v_pk_mul_f32 v[46:47], v[150:151], v[168:169] op_sel_hi:[1,0]
	v_pk_mul_f32 v[48:49], v[150:151], v[176:177] op_sel_hi:[1,0]
	v_pk_fma_f32 v[46:47], v[152:153], v[168:169], v[46:47] op_sel:[0,1,0]
	v_pk_fma_f32 v[48:49], v[152:153], v[176:177], v[48:49] op_sel:[0,1,0]
	v_pk_fma_f32 v[46:47], v[154:155], v[170:171], v[46:47] op_sel_hi:[1,0,1]
	v_pk_fma_f32 v[48:49], v[154:155], v[178:179], v[48:49] op_sel_hi:[1,0,1]
	v_pk_fma_f32 v[46:47], v[156:157], v[170:171], v[46:47] op_sel:[0,1,0]
	v_pk_fma_f32 v[48:49], v[156:157], v[178:179], v[48:49] op_sel:[0,1,0]
	v_pk_fma_f32 v[46:47], v[158:159], v[172:173], v[46:47] op_sel_hi:[1,0,1]
	v_pk_fma_f32 v[48:49], v[158:159], v[180:181], v[48:49] op_sel_hi:[1,0,1]
	v_pk_fma_f32 v[46:47], v[160:161], v[172:173], v[46:47] op_sel:[0,1,0]
	v_pk_fma_f32 v[48:49], v[160:161], v[180:181], v[48:49] op_sel:[0,1,0]
	v_pk_fma_f32 v[46:47], v[162:163], v[174:175], v[46:47] op_sel_hi:[1,0,1]
	v_pk_fma_f32 v[48:49], v[162:163], v[182:183], v[48:49] op_sel_hi:[1,0,1]
	v_pk_fma_f32 v[46:47], v[164:165], v[174:175], v[46:47] op_sel:[0,1,0]
	v_pk_fma_f32 v[48:49], v[164:165], v[182:183], v[48:49] op_sel:[0,1,0]
	v_pk_mul_f32 v[150:151], v[150:151], v[184:185] op_sel_hi:[1,0]
	v_pk_mul_f32 v[152:153], v[152:153], v[184:185] op_sel:[0,1]
	v_pk_mul_f32 v[154:155], v[154:155], v[186:187] op_sel_hi:[1,0]
	v_pk_mul_f32 v[156:157], v[156:157], v[186:187] op_sel:[0,1]
	v_pk_mul_f32 v[158:159], v[158:159], v[188:189] op_sel_hi:[1,0]
	v_pk_mul_f32 v[160:161], v[160:161], v[188:189] op_sel:[0,1]
	v_pk_mul_f32 v[162:163], v[162:163], v[190:191] op_sel_hi:[1,0]
	v_pk_mul_f32 v[164:165], v[164:165], v[190:191] op_sel:[0,1]
	v_add_f32_dpp v46, v46, v46 quad_perm:[1,0,3,2] row_mask:0xf bank_mask:0xf bound_ctrl:1
	v_add_f32_dpp v47, v47, v47 quad_perm:[1,0,3,2] row_mask:0xf bank_mask:0xf bound_ctrl:1
	v_add_f32_dpp v48, v48, v48 quad_perm:[1,0,3,2] row_mask:0xf bank_mask:0xf bound_ctrl:1
	v_add_f32_dpp v49, v49, v49 quad_perm:[1,0,3,2] row_mask:0xf bank_mask:0xf bound_ctrl:1
	v_add_f32_dpp v46, v46, v46 quad_perm:[2,3,0,1] row_mask:0xf bank_mask:0xf bound_ctrl:1
	v_add_f32_dpp v47, v47, v47 quad_perm:[2,3,0,1] row_mask:0xf bank_mask:0xf bound_ctrl:1
	v_add_f32_dpp v48, v48, v48 quad_perm:[2,3,0,1] row_mask:0xf bank_mask:0xf bound_ctrl:1
	v_add_f32_dpp v49, v49, v49 quad_perm:[2,3,0,1] row_mask:0xf bank_mask:0xf bound_ctrl:1
	v_add_f32_dpp v46, v46, v46 row_half_mirror row_mask:0xf bank_mask:0xf bound_ctrl:1
	v_add_f32_dpp v47, v47, v47 row_half_mirror row_mask:0xf bank_mask:0xf bound_ctrl:1
	v_add_f32_dpp v48, v48, v48 row_half_mirror row_mask:0xf bank_mask:0xf bound_ctrl:1
	v_add_f32_dpp v49, v49, v49 row_half_mirror row_mask:0xf bank_mask:0xf bound_ctrl:1
	v_pk_fma_f32 v[48:49], v[46:47], v[216:217], v[48:49] op_sel_hi:[1,0,1]
	v_pk_fma_f32 v[48:49], v[212:213], v[216:217], v[48:49] op_sel:[0,1,0]
	s_mov_b64 exec, s[100:101]
	ds_write_b64 v53, v[48:49] offset:0
	s_mov_b64 exec, -1
	v_pk_fma_f32 v[150:151], v[46:47], v[192:193], v[150:151] op_sel_hi:[1,0,1]
	v_pk_fma_f32 v[152:153], v[46:47], v[192:193], v[152:153] op_sel:[0,1,0]
	v_pk_fma_f32 v[154:155], v[46:47], v[194:195], v[154:155] op_sel_hi:[1,0,1]
	v_pk_fma_f32 v[156:157], v[46:47], v[194:195], v[156:157] op_sel:[0,1,0]
	v_pk_fma_f32 v[158:159], v[46:47], v[196:197], v[158:159] op_sel_hi:[1,0,1]
	v_pk_fma_f32 v[160:161], v[46:47], v[196:197], v[160:161] op_sel:[0,1,0]
	v_pk_fma_f32 v[162:163], v[46:47], v[198:199], v[162:163] op_sel_hi:[1,0,1]
	v_pk_fma_f32 v[164:165], v[46:47], v[198:199], v[164:165] op_sel:[0,1,0]
	v_pk_fma_f32 v[150:151], v[212:213], v[200:201], v[150:151] op_sel_hi:[1,0,1]
	v_pk_fma_f32 v[152:153], v[212:213], v[200:201], v[152:153] op_sel:[0,1,0]
	v_pk_fma_f32 v[154:155], v[212:213], v[202:203], v[154:155] op_sel_hi:[1,0,1]
	v_pk_fma_f32 v[156:157], v[212:213], v[202:203], v[156:157] op_sel:[0,1,0]
	v_pk_fma_f32 v[158:159], v[212:213], v[204:205], v[158:159] op_sel_hi:[1,0,1]
	v_pk_fma_f32 v[160:161], v[212:213], v[204:205], v[160:161] op_sel:[0,1,0]
	v_pk_fma_f32 v[162:163], v[212:213], v[206:207], v[162:163] op_sel_hi:[1,0,1]
	v_pk_fma_f32 v[164:165], v[212:213], v[206:207], v[164:165] op_sel:[0,1,0]
	s_waitcnt lgkmcnt(0)
; #define LAS __attribute__((address_space(3)))
; template <class AT_>
; __device__ __forceinline__ void rwkv_scan_phase(const AT_& a, Frame& F, int j) {
;     ...
;                     auto ld = [&](int t) { RwOps o; const LAS float* p = ob + t * 64 + 8 * kg;
;                         o.a0 = *(const LAS f32x4*)p; o.a1 = *(const LAS f32x4*)(p + 4); p += RW_T * 64; o.r0 = *(const LAS f32x4*)p; o.r1 = *(const LAS f32x4*)(p + 4); p += RW_T * 64;
;                         o.w0 = *(const LAS f32x4*)p; o.w1 = *(const LAS f32x4*)(p + 4); p += RW_T * 64; o.b0 = *(const LAS f32x4*)p; o.b1 = *(const LAS f32x4*)(p + 4); p += RW_T * 64;
;                         o.k0 = *(const LAS f32x4*)p; o.k1 = *(const LAS f32x4*)(p + 4);
;                         o.v = *(const LAS f32x2*)(ob + 5 * RW_T * 64 + t * 64 + v0); o.sc = *(const LAS f32x2*)(ob + 6 * RW_T * 64 + t * 4); return o; };
;                     auto step = [&](const RwOps& cur, int t) {
;                         const f32x2 a01 = {cur.a0.x, cur.a0.y}, a23 = {cur.a0.z, cur.a0.w}, a45 = {cur.a1.x, cur.a1.y}, a67 = {cur.a1.z, cur.a1.w};
;                         const f32x2 r01 = {cur.r0.x, cur.r0.y}, r23 = {cur.r0.z, cur.r0.w}, r45 = {cur.r1.x, cur.r1.y}, r67 = {cur.r1.z, cur.r1.w};
;                         f32x2 sA0 = S0[0] * a01, sA1 = S1[0] * a01, sY0 = S0[0] * r01, sY1 = S1[0] * r01;
;                         sA0 = S0[1] * a23 + sA0; sA1 = S1[1] * a23 + sA1; sY0 = S0[1] * r23 + sY0; sY1 = S1[1] * r23 + sY1;
;                         sA0 = S0[2] * a45 + sA0; sA1 = S1[2] * a45 + sA1; sY0 = S0[2] * r45 + sY0; sY1 = S1[2] * r45 + sY1;
;                         sA0 = S0[3] * a67 + sA0; sA1 = S1[3] * a67 + sA1; sY0 = S0[3] * r67 + sY0; sY1 = S1[3] * r67 + sY1;
;                         const float sa0 = row8_allsum(sA0.x + sA0.y), sa1 = row8_allsum(sA1.x + sA1.y), yy0 = row8_allsum(sY0.x + sY0.y), yy1 = row8_allsum(sY1.x + sY1.y);
;                         if (kg == 0) { f32x2 yo; yo.x = yy0 + sa0 * cur.sc.x + cur.v.x * cur.sc.y; yo.y = yy1 + sa1 * cur.sc.x + cur.v.y * cur.sc.y; *(LAS f32x2*)(Yb + t * 64 + v0) = yo; }
;                         const f32x2 w01 = {cur.w0.x, cur.w0.y}, w23 = {cur.w0.z, cur.w0.w}, w45 = {cur.w1.x, cur.w1.y}, w67 = {cur.w1.z, cur.w1.w};
;                         const f32x2 b01 = {cur.b0.x, cur.b0.y}, b23 = {cur.b0.z, cur.b0.w}, b45 = {cur.b1.x, cur.b1.y}, b67 = {cur.b1.z, cur.b1.w};
	ds_read_b128 v[168:171], v50 offset:512
	ds_read_b128 v[172:175], v50 offset:528
	ds_read_b128 v[176:179], v50 offset:8704
	ds_read_b128 v[180:183], v50 offset:8720
	ds_read_b128 v[184:187], v50 offset:16896
	ds_read_b128 v[188:191], v50 offset:16912
	ds_read_b128 v[192:195], v50 offset:25088
	ds_read_b128 v[196:199], v50 offset:25104
	ds_read_b128 v[200:203], v50 offset:33280
	ds_read_b128 v[204:207], v50 offset:33296
	v_pk_mul_f32 v[46:47], v[150:151], v[2:3] op_sel_hi:[1,0]
	v_pk_mul_f32 v[48:49], v[150:151], v[10:11] op_sel_hi:[1,0]
	v_pk_fma_f32 v[46:47], v[152:153], v[2:3], v[46:47] op_sel:[0,1,0]
	v_pk_fma_f32 v[48:49], v[152:153], v[10:11], v[48:49] op_sel:[0,1,0]
	v_pk_fma_f32 v[46:47], v[154:155], v[4:5], v[46:47] op_sel_hi:[1,0,1]
	v_pk_fma_f32 v[48:49], v[154:155], v[12:13], v[48:49] op_sel_hi:[1,0,1]
	v_pk_fma_f32 v[46:47], v[156:157], v[4:5], v[46:47] op_sel:[0,1,0]
	v_pk_fma_f32 v[48:49], v[156:157], v[12:13], v[48:49] op_sel:[0,1,0]
	v_pk_fma_f32 v[46:47], v[158:159], v[6:7], v[46:47] op_sel_hi:[1,0,1]
	v_pk_fma_f32 v[48:49], v[158:159], v[14:15], v[48:49] op_sel_hi:[1,0,1]
	v_pk_fma_f32 v[46:47], v[160:161], v[6:7], v[46:47] op_sel:[0,1,0]
	v_pk_fma_f32 v[48:49], v[160:161], v[14:15], v[48:49] op_sel:[0,1,0]
	v_pk_fma_f32 v[46:47], v[162:163], v[8:9], v[46:47] op_sel_hi:[1,0,1]
	v_pk_fma_f32 v[48:49], v[162:163], v[16:17], v[48:49] op_sel_hi:[1,0,1]
	v_pk_fma_f32 v[46:47], v[164:165], v[8:9], v[46:47] op_sel:[0,1,0]
	v_pk_fma_f32 v[48:49], v[164:165], v[16:17], v[48:49] op_sel:[0,1,0]
	v_pk_mul_f32 v[150:151], v[150:151], v[18:19] op_sel_hi:[1,0]
	v_pk_mul_f32 v[152:153], v[152:153], v[18:19] op_sel:[0,1]
	v_pk_mul_f32 v[154:155], v[154:155], v[20:21] op_sel_hi:[1,0]
	v_pk_mul_f32 v[156:157], v[156:157], v[20:21] op_sel:[0,1]
	v_pk_mul_f32 v[158:159], v[158:159], v[22:23] op_sel_hi:[1,0]
	v_pk_mul_f32 v[160:161], v[160:161], v[22:23] op_sel:[0,1]
	v_pk_mul_f32 v[162:163], v[162:163], v[24:25] op_sel_hi:[1,0]
	v_pk_mul_f32 v[164:165], v[164:165], v[24:25] op_sel:[0,1]
	v_add_f32_dpp v46, v46, v46 quad_perm:[1,0,3,2] row_mask:0xf bank_mask:0xf bound_ctrl:1
	v_add_f32_dpp v47, v47, v47 quad_perm:[1,0,3,2] row_mask:0xf bank_mask:0xf bound_ctrl:1
	v_add_f32_dpp v48, v48, v48 quad_perm:[1,0,3,2] row_mask:0xf bank_mask:0xf bound_ctrl:1
	v_add_f32_dpp v49, v49, v49 quad_perm:[1,0,3,2] row_mask:0xf bank_mask:0xf bound_ctrl:1
	v_add_f32_dpp v46, v46, v46 quad_perm:[2,3,0,1] row_mask:0xf bank_mask:0xf bound_ctrl:1
	v_add_f32_dpp v47, v47, v47 quad_perm:[2,3,0,1] row_mask:0xf bank_mask:0xf bound_ctrl:1
	v_add_f32_dpp v48, v48, v48 quad_perm:[2,3,0,1] row_mask:0xf bank_mask:0xf bound_ctrl:1
	v_add_f32_dpp v49, v49, v49 quad_perm:[2,3,0,1] row_mask:0xf bank_mask:0xf bound_ctrl:1
	v_add_f32_dpp v46, v46, v46 row_half_mirror row_mask:0xf bank_mask:0xf bound_ctrl:1
	v_add_f32_dpp v47, v47, v47 row_half_mirror row_mask:0xf bank_mask:0xf bound_ctrl:1
	v_add_f32_dpp v48, v48, v48 row_half_mirror row_mask:0xf bank_mask:0xf bound_ctrl:1
	v_add_f32_dpp v49, v49, v49 row_half_mirror row_mask:0xf bank_mask:0xf bound_ctrl:1
	v_pk_fma_f32 v[48:49], v[46:47], v[218:219], v[48:49] op_sel_hi:[1,0,1]
	v_pk_fma_f32 v[48:49], v[214:215], v[218:219], v[48:49] op_sel:[0,1,0]
	s_mov_b64 exec, s[100:101]
	ds_write_b64 v53, v[48:49] offset:256
	s_mov_b64 exec, -1
	v_pk_fma_f32 v[150:151], v[46:47], v[26:27], v[150:151] op_sel_hi:[1,0,1]
	v_pk_fma_f32 v[152:153], v[46:47], v[26:27], v[152:153] op_sel:[0,1,0]
	v_pk_fma_f32 v[154:155], v[46:47], v[28:29], v[154:155] op_sel_hi:[1,0,1]
	v_pk_fma_f32 v[156:157], v[46:47], v[28:29], v[156:157] op_sel:[0,1,0]
	v_pk_fma_f32 v[158:159], v[46:47], v[30:31], v[158:159] op_sel_hi:[1,0,1]
	v_pk_fma_f32 v[160:161], v[46:47], v[30:31], v[160:161] op_sel:[0,1,0]
	v_pk_fma_f32 v[162:163], v[46:47], v[32:33], v[162:163] op_sel_hi:[1,0,1]
	v_pk_fma_f32 v[164:165], v[46:47], v[32:33], v[164:165] op_sel:[0,1,0]
	v_pk_fma_f32 v[150:151], v[214:215], v[34:35], v[150:151] op_sel_hi:[1,0,1]
	v_pk_fma_f32 v[152:153], v[214:215], v[34:35], v[152:153] op_sel:[0,1,0]
	v_pk_fma_f32 v[154:155], v[214:215], v[36:37], v[154:155] op_sel_hi:[1,0,1]
	v_pk_fma_f32 v[156:157], v[214:215], v[36:37], v[156:157] op_sel:[0,1,0]
	v_pk_fma_f32 v[158:159], v[214:215], v[38:39], v[158:159] op_sel_hi:[1,0,1]
	v_pk_fma_f32 v[160:161], v[214:215], v[38:39], v[160:161] op_sel:[0,1,0]
	v_pk_fma_f32 v[162:163], v[214:215], v[40:41], v[162:163] op_sel_hi:[1,0,1]
	v_pk_fma_f32 v[164:165], v[214:215], v[40:41], v[164:165] op_sel:[0,1,0]
	s_waitcnt lgkmcnt(0)
; #define LAS __attribute__((address_space(3)))
; template <class AT_>
; __device__ __forceinline__ void rwkv_scan_phase(const AT_& a, Frame& F, int j) {
;     ...
;                     auto ld = [&](int t) { RwOps o; const LAS float* p = ob + t * 64 + 8 * kg;
;                         o.a0 = *(const LAS f32x4*)p; o.a1 = *(const LAS f32x4*)(p + 4); p += RW_T * 64; o.r0 = *(const LAS f32x4*)p; o.r1 = *(const LAS f32x4*)(p + 4); p += RW_T * 64;
;                         o.w0 = *(const LAS f32x4*)p; o.w1 = *(const LAS f32x4*)(p + 4); p += RW_T * 64; o.b0 = *(const LAS f32x4*)p; o.b1 = *(const LAS f32x4*)(p + 4); p += RW_T * 64;
;                         o.k0 = *(const LAS f32x4*)p; o.k1 = *(const LAS f32x4*)(p + 4);
;                         o.v = *(const LAS f32x2*)(ob + 5 * RW_T * 64 + t * 64 + v0); o.sc = *(const LAS f32x2*)(ob + 6 * RW_T * 64 + t * 4); return o; };
;                     auto step = [&](const RwOps& cur, int t) {
;                         const f32x2 a01 = {cur.a0.x, cur.a0.y}, a23 = {cur.a0.z, cur.a0.w}, a45 = {cur.a1.x, cur.a1.y}, a67 = {cur.a1.z, cur.a1.w};
;                         const f32x2 r01 = {cur.r0.x, cur.r0.y}, r23 = {cur.r0.z, cur.r0.w}, r45 = {cur.r1.x, cur.r1.y}, r67 = {cur.r1.z, cur.r1.w};
;                         f32x2 sA0 = S0[0] * a01, sA1 = S1[0] * a01, sY0 = S0[0] * r01, sY1 = S1[0] * r01;
;                         sA0 = S0[1] * a23 + sA0; sA1 = S1[1] * a23 + sA1; sY0 = S0[1] * r23 + sY0; sY1 = S1[1] * r23 + sY1;
;                         sA0 = S0[2] * a45 + sA0; sA1 = S1[2] * a45 + sA1; sY0 = S0[2] * r45 + sY0; sY1 = S1[2] * r45 + sY1;
;                         sA0 = S0[3] * a67 + sA0; sA1 = S1[3] * a67 + sA1; sY0 = S0[3] * r67 + sY0; sY1 = S1[3] * r67 + sY1;
;                         const float sa0 = row8_allsum(sA0.x + sA0.y), sa1 = row8_allsum(sA1.x + sA1.y), yy0 = row8_allsum(sY0.x + sY0.y), yy1 = row8_allsum(sY1.x + sY1.y);
;                         if (kg == 0) { f32x2 yo; yo.x = yy0 + sa0 * cur.sc.x + cur.v.x * cur.sc.y; yo.y = yy1 + sa1 * cur.sc.x + cur.v.y * cur.sc.y; *(LAS f32x2*)(Yb + t * 64 + v0) = yo; }
;                         const f32x2 w01 = {cur.w0.x, cur.w0.y}, w23 = {cur.w0.z, cur.w0.w}, w45 = {cur.w1.x, cur.w1.y}, w67 = {cur.w1.z, cur.w1.w};
;                         const f32x2 b01 = {cur.b0.x, cur.b0.y}, b23 = {cur.b0.z, cur.b0.w}, b45 = {cur.b1.x, cur.b1.y}, b67 = {cur.b1.z, cur.b1.w};
	ds_read_b128 v[2:5], v50 offset:768
	ds_read_b128 v[6:9], v50 offset:784
	ds_read_b128 v[10:13], v50 offset:8960
	ds_read_b128 v[14:17], v50 offset:8976
	ds_read_b128 v[18:21], v50 offset:17152
	ds_read_b128 v[22:25], v50 offset:17168
	ds_read_b128 v[26:29], v50 offset:25344
	ds_read_b128 v[30:33], v50 offset:25360
	ds_read_b128 v[34:37], v50 offset:33536
	ds_read_b128 v[38:41], v50 offset:33552
	ds_read2_b64 v[212:215], v51 offset0:64 offset1:96
	ds_read2_b64 v[216:219], v52 offset0:4 offset1:6
	v_pk_mul_f32 v[46:47], v[150:151], v[168:169] op_sel_hi:[1,0]
	v_pk_mul_f32 v[48:49], v[150:151], v[176:177] op_sel_hi:[1,0]
	v_pk_fma_f32 v[46:47], v[152:153], v[168:169], v[46:47] op_sel:[0,1,0]
	v_pk_fma_f32 v[48:49], v[152:153], v[176:177], v[48:49] op_sel:[0,1,0]
	v_pk_fma_f32 v[46:47], v[154:155], v[170:171], v[46:47] op_sel_hi:[1,0,1]
	v_pk_fma_f32 v[48:49], v[154:155], v[178:179], v[48:49] op_sel_hi:[1,0,1]
	v_pk_fma_f32 v[46:47], v[156:157], v[170:171], v[46:47] op_sel:[0,1,0]
	v_pk_fma_f32 v[48:49], v[156:157], v[178:179], v[48:49] op_sel:[0,1,0]
	v_pk_fma_f32 v[46:47], v[158:159], v[172:173], v[46:47] op_sel_hi:[1,0,1]
	v_pk_fma_f32 v[48:49], v[158:159], v[180:181], v[48:49] op_sel_hi:[1,0,1]
	v_pk_fma_f32 v[46:47], v[160:161], v[172:173], v[46:47] op_sel:[0,1,0]
	v_pk_fma_f32 v[48:49], v[160:161], v[180:181], v[48:49] op_sel:[0,1,0]
	v_pk_fma_f32 v[46:47], v[162:163], v[174:175], v[46:47] op_sel_hi:[1,0,1]
	v_pk_fma_f32 v[48:49], v[162:163], v[182:183], v[48:49] op_sel_hi:[1,0,1]
	v_pk_fma_f32 v[46:47], v[164:165], v[174:175], v[46:47] op_sel:[0,1,0]
	v_pk_fma_f32 v[48:49], v[164:165], v[182:183], v[48:49] op_sel:[0,1,0]
	v_pk_mul_f32 v[150:151], v[150:151], v[184:185] op_sel_hi:[1,0]
	v_pk_mul_f32 v[152:153], v[152:153], v[184:185] op_sel:[0,1]
	v_pk_mul_f32 v[154:155], v[154:155], v[186:187] op_sel_hi:[1,0]
	v_pk_mul_f32 v[156:157], v[156:157], v[186:187] op_sel:[0,1]
	v_pk_mul_f32 v[158:159], v[158:159], v[188:189] op_sel_hi:[1,0]
	v_pk_mul_f32 v[160:161], v[160:161], v[188:189] op_sel:[0,1]
	v_pk_mul_f32 v[162:163], v[162:163], v[190:191] op_sel_hi:[1,0]
	v_pk_mul_f32 v[164:165], v[164:165], v[190:191] op_sel:[0,1]
	v_add_f32_dpp v46, v46, v46 quad_perm:[1,0,3,2] row_mask:0xf bank_mask:0xf bound_ctrl:1
	v_add_f32_dpp v47, v47, v47 quad_perm:[1,0,3,2] row_mask:0xf bank_mask:0xf bound_ctrl:1
	v_add_f32_dpp v48, v48, v48 quad_perm:[1,0,3,2] row_mask:0xf bank_mask:0xf bound_ctrl:1
	v_add_f32_dpp v49, v49, v49 quad_perm:[1,0,3,2] row_mask:0xf bank_mask:0xf bound_ctrl:1
	v_add_f32_dpp v46, v46, v46 quad_perm:[2,3,0,1] row_mask:0xf bank_mask:0xf bound_ctrl:1
	v_add_f32_dpp v47, v47, v47 quad_perm:[2,3,0,1] row_mask:0xf bank_mask:0xf bound_ctrl:1
	v_add_f32_dpp v48, v48, v48 quad_perm:[2,3,0,1] row_mask:0xf bank_mask:0xf bound_ctrl:1
	v_add_f32_dpp v49, v49, v49 quad_perm:[2,3,0,1] row_mask:0xf bank_mask:0xf bound_ctrl:1
	v_add_f32_dpp v46, v46, v46 row_half_mirror row_mask:0xf bank_mask:0xf bound_ctrl:1
	v_add_f32_dpp v47, v47, v47 row_half_mirror row_mask:0xf bank_mask:0xf bound_ctrl:1
	v_add_f32_dpp v48, v48, v48 row_half_mirror row_mask:0xf bank_mask:0xf bound_ctrl:1
	v_add_f32_dpp v49, v49, v49 row_half_mirror row_mask:0xf bank_mask:0xf bound_ctrl:1
	v_pk_fma_f32 v[48:49], v[46:47], v[224:225], v[48:49] op_sel_hi:[1,0,1]
	v_pk_fma_f32 v[48:49], v[220:221], v[224:225], v[48:49] op_sel:[0,1,0]
	s_mov_b64 exec, s[100:101]
	ds_write_b64 v53, v[48:49] offset:512
	s_mov_b64 exec, -1
	v_pk_fma_f32 v[150:151], v[46:47], v[192:193], v[150:151] op_sel_hi:[1,0,1]
	v_pk_fma_f32 v[152:153], v[46:47], v[192:193], v[152:153] op_sel:[0,1,0]
	v_pk_fma_f32 v[154:155], v[46:47], v[194:195], v[154:155] op_sel_hi:[1,0,1]
	v_pk_fma_f32 v[156:157], v[46:47], v[194:195], v[156:157] op_sel:[0,1,0]
	v_pk_fma_f32 v[158:159], v[46:47], v[196:197], v[158:159] op_sel_hi:[1,0,1]
	v_pk_fma_f32 v[160:161], v[46:47], v[196:197], v[160:161] op_sel:[0,1,0]
	v_pk_fma_f32 v[162:163], v[46:47], v[198:199], v[162:163] op_sel_hi:[1,0,1]
	v_pk_fma_f32 v[164:165], v[46:47], v[198:199], v[164:165] op_sel:[0,1,0]
	v_pk_fma_f32 v[150:151], v[220:221], v[200:201], v[150:151] op_sel_hi:[1,0,1]
	v_pk_fma_f32 v[152:153], v[220:221], v[200:201], v[152:153] op_sel:[0,1,0]
	v_pk_fma_f32 v[154:155], v[220:221], v[202:203], v[154:155] op_sel_hi:[1,0,1]
	v_pk_fma_f32 v[156:157], v[220:221], v[202:203], v[156:157] op_sel:[0,1,0]
	v_pk_fma_f32 v[158:159], v[220:221], v[204:205], v[158:159] op_sel_hi:[1,0,1]
	v_pk_fma_f32 v[160:161], v[220:221], v[204:205], v[160:161] op_sel:[0,1,0]
	v_pk_fma_f32 v[162:163], v[220:221], v[206:207], v[162:163] op_sel_hi:[1,0,1]
	v_pk_fma_f32 v[164:165], v[220:221], v[206:207], v[164:165] op_sel:[0,1,0]
	s_waitcnt lgkmcnt(0)
; #define LAS __attribute__((address_space(3)))
; template <class AT_>
; __device__ __forceinline__ void rwkv_scan_phase(const AT_& a, Frame& F, int j) {
;     ...
;                     auto ld = [&](int t) { RwOps o; const LAS float* p = ob + t * 64 + 8 * kg;
;                         o.a0 = *(const LAS f32x4*)p; o.a1 = *(const LAS f32x4*)(p + 4); p += RW_T * 64; o.r0 = *(const LAS f32x4*)p; o.r1 = *(const LAS f32x4*)(p + 4); p += RW_T * 64;
;                         o.w0 = *(const LAS f32x4*)p; o.w1 = *(const LAS f32x4*)(p + 4); p += RW_T * 64; o.b0 = *(const LAS f32x4*)p; o.b1 = *(const LAS f32x4*)(p + 4); p += RW_T * 64;
;                         o.k0 = *(const LAS f32x4*)p; o.k1 = *(const LAS f32x4*)(p + 4);
;                         o.v = *(const LAS f32x2*)(ob + 5 * RW_T * 64 + t * 64 + v0); o.sc = *(const LAS f32x2*)(ob + 6 * RW_T * 64 + t * 4); return o; };
;                     auto step = [&](const RwOps& cur, int t) {
;                         const f32x2 a01 = {cur.a0.x, cur.a0.y}, a23 = {cur.a0.z, cur.a0.w}, a45 = {cur.a1.x, cur.a1.y}, a67 = {cur.a1.z, cur.a1.w};
;                         const f32x2 r01 = {cur.r0.x, cur.r0.y}, r23 = {cur.r0.z, cur.r0.w}, r45 = {cur.r1.x, cur.r1.y}, r67 = {cur.r1.z, cur.r1.w};
;                         f32x2 sA0 = S0[0] * a01, sA1 = S1[0] * a01, sY0 = S0[0] * r01, sY1 = S1[0] * r01;
;                         sA0 = S0[1] * a23 + sA0; sA1 = S1[1] * a23 + sA1; sY0 = S0[1] * r23 + sY0; sY1 = S1[1] * r23 + sY1;
;                         sA0 = S0[2] * a45 + sA0; sA1 = S1[2] * a45 + sA1; sY0 = S0[2] * r45 + sY0; sY1 = S1[2] * r45 + sY1;
;                         sA0 = S0[3] * a67 + sA0; sA1 = S1[3] * a67 + sA1; sY0 = S0[3] * r67 + sY0; sY1 = S1[3] * r67 + sY1;
;                         const float sa0 = row8_allsum(sA0.x + sA0.y), sa1 = row8_allsum(sA1.x + sA1.y), yy0 = row8_allsum(sY0.x + sY0.y), yy1 = row8_allsum(sY1.x + sY1.y);
;                         if (kg == 0) { f32x2 yo; yo.x = yy0 + sa0 * cur.sc.x + cur.v.x * cur.sc.y; yo.y = yy1 + sa1 * cur.sc.x + cur.v.y * cur.sc.y; *(LAS f32x2*)(Yb + t * 64 + v0) = yo; }
;                         const f32x2 w01 = {cur.w0.x, cur.w0.y}, w23 = {cur.w0.z, cur.w0.w}, w45 = {cur.w1.x, cur.w1.y}, w67 = {cur.w1.z, cur.w1.w};
;                         const f32x2 b01 = {cur.b0.x, cur.b0.y}, b23 = {cur.b0.z, cur.b0.w}, b45 = {cur.b1.x, cur.b1.y}, b67 = {cur.b1.z, cur.b1.w};
	ds_read_b128 v[168:171], v50 offset:1024
	ds_read_b128 v[172:175], v50 offset:1040
	ds_read_b128 v[176:179], v50 offset:9216
	ds_read_b128 v[180:183], v50 offset:9232
	ds_read_b128 v[184:187], v50 offset:17408
	ds_read_b128 v[188:191], v50 offset:17424
	ds_read_b128 v[192:195], v50 offset:25600
	ds_read_b128 v[196:199], v50 offset:25616
	ds_read_b128 v[200:203], v50 offset:33792
	ds_read_b128 v[204:207], v50 offset:33808
	v_pk_mul_f32 v[46:47], v[150:151], v[2:3] op_sel_hi:[1,0]
	v_pk_mul_f32 v[48:49], v[150:151], v[10:11] op_sel_hi:[1,0]
	v_pk_fma_f32 v[46:47], v[152:153], v[2:3], v[46:47] op_sel:[0,1,0]
	v_pk_fma_f32 v[48:49], v[152:153], v[10:11], v[48:49] op_sel:[0,1,0]
	v_pk_fma_f32 v[46:47], v[154:155], v[4:5], v[46:47] op_sel_hi:[1,0,1]
	v_pk_fma_f32 v[48:49], v[154:155], v[12:13], v[48:49] op_sel_hi:[1,0,1]
	v_pk_fma_f32 v[46:47], v[156:157], v[4:5], v[46:47] op_sel:[0,1,0]
	v_pk_fma_f32 v[48:49], v[156:157], v[12:13], v[48:49] op_sel:[0,1,0]
	v_pk_fma_f32 v[46:47], v[158:159], v[6:7], v[46:47] op_sel_hi:[1,0,1]
	v_pk_fma_f32 v[48:49], v[158:159], v[14:15], v[48:49] op_sel_hi:[1,0,1]
	v_pk_fma_f32 v[46:47], v[160:161], v[6:7], v[46:47] op_sel:[0,1,0]
	v_pk_fma_f32 v[48:49], v[160:161], v[14:15], v[48:49] op_sel:[0,1,0]
	v_pk_fma_f32 v[46:47], v[162:163], v[8:9], v[46:47] op_sel_hi:[1,0,1]
	v_pk_fma_f32 v[48:49], v[162:163], v[16:17], v[48:49] op_sel_hi:[1,0,1]
	v_pk_fma_f32 v[46:47], v[164:165], v[8:9], v[46:47] op_sel:[0,1,0]
	v_pk_fma_f32 v[48:49], v[164:165], v[16:17], v[48:49] op_sel:[0,1,0]
	v_pk_mul_f32 v[150:151], v[150:151], v[18:19] op_sel_hi:[1,0]
	v_pk_mul_f32 v[152:153], v[152:153], v[18:19] op_sel:[0,1]
	v_pk_mul_f32 v[154:155], v[154:155], v[20:21] op_sel_hi:[1,0]
	v_pk_mul_f32 v[156:157], v[156:157], v[20:21] op_sel:[0,1]
	v_pk_mul_f32 v[158:159], v[158:159], v[22:23] op_sel_hi:[1,0]
	v_pk_mul_f32 v[160:161], v[160:161], v[22:23] op_sel:[0,1]
	v_pk_mul_f32 v[162:163], v[162:163], v[24:25] op_sel_hi:[1,0]
	v_pk_mul_f32 v[164:165], v[164:165], v[24:25] op_sel:[0,1]
	v_add_f32_dpp v46, v46, v46 quad_perm:[1,0,3,2] row_mask:0xf bank_mask:0xf bound_ctrl:1
	v_add_f32_dpp v47, v47, v47 quad_perm:[1,0,3,2] row_mask:0xf bank_mask:0xf bound_ctrl:1
	v_add_f32_dpp v48, v48, v48 quad_perm:[1,0,3,2] row_mask:0xf bank_mask:0xf bound_ctrl:1
	v_add_f32_dpp v49, v49, v49 quad_perm:[1,0,3,2] row_mask:0xf bank_mask:0xf bound_ctrl:1
	v_add_f32_dpp v46, v46, v46 quad_perm:[2,3,0,1] row_mask:0xf bank_mask:0xf bound_ctrl:1
	v_add_f32_dpp v47, v47, v47 quad_perm:[2,3,0,1] row_mask:0xf bank_mask:0xf bound_ctrl:1
	v_add_f32_dpp v48, v48, v48 quad_perm:[2,3,0,1] row_mask:0xf bank_mask:0xf bound_ctrl:1
	v_add_f32_dpp v49, v49, v49 quad_perm:[2,3,0,1] row_mask:0xf bank_mask:0xf bound_ctrl:1
	v_add_f32_dpp v46, v46, v46 row_half_mirror row_mask:0xf bank_mask:0xf bound_ctrl:1
	v_add_f32_dpp v47, v47, v47 row_half_mirror row_mask:0xf bank_mask:0xf bound_ctrl:1
	v_add_f32_dpp v48, v48, v48 row_half_mirror row_mask:0xf bank_mask:0xf bound_ctrl:1
	v_add_f32_dpp v49, v49, v49 row_half_mirror row_mask:0xf bank_mask:0xf bound_ctrl:1
	v_pk_fma_f32 v[48:49], v[46:47], v[226:227], v[48:49] op_sel_hi:[1,0,1]
	v_pk_fma_f32 v[48:49], v[222:223], v[226:227], v[48:49] op_sel:[0,1,0]
	s_mov_b64 exec, s[100:101]
	ds_write_b64 v53, v[48:49] offset:768
	s_mov_b64 exec, -1
	v_pk_fma_f32 v[150:151], v[46:47], v[26:27], v[150:151] op_sel_hi:[1,0,1]
	v_pk_fma_f32 v[152:153], v[46:47], v[26:27], v[152:153] op_sel:[0,1,0]
	v_pk_fma_f32 v[154:155], v[46:47], v[28:29], v[154:155] op_sel_hi:[1,0,1]
	v_pk_fma_f32 v[156:157], v[46:47], v[28:29], v[156:157] op_sel:[0,1,0]
	v_pk_fma_f32 v[158:159], v[46:47], v[30:31], v[158:159] op_sel_hi:[1,0,1]
	v_pk_fma_f32 v[160:161], v[46:47], v[30:31], v[160:161] op_sel:[0,1,0]
	v_pk_fma_f32 v[162:163], v[46:47], v[32:33], v[162:163] op_sel_hi:[1,0,1]
	v_pk_fma_f32 v[164:165], v[46:47], v[32:33], v[164:165] op_sel:[0,1,0]
	v_pk_fma_f32 v[150:151], v[222:223], v[34:35], v[150:151] op_sel_hi:[1,0,1]
	v_pk_fma_f32 v[152:153], v[222:223], v[34:35], v[152:153] op_sel:[0,1,0]
	v_pk_fma_f32 v[154:155], v[222:223], v[36:37], v[154:155] op_sel_hi:[1,0,1]
	v_pk_fma_f32 v[156:157], v[222:223], v[36:37], v[156:157] op_sel:[0,1,0]
	v_pk_fma_f32 v[158:159], v[222:223], v[38:39], v[158:159] op_sel_hi:[1,0,1]
	v_pk_fma_f32 v[160:161], v[222:223], v[38:39], v[160:161] op_sel:[0,1,0]
	v_pk_fma_f32 v[162:163], v[222:223], v[40:41], v[162:163] op_sel_hi:[1,0,1]
	v_pk_fma_f32 v[164:165], v[222:223], v[40:41], v[164:165] op_sel:[0,1,0]
	s_waitcnt lgkmcnt(0)
; #define LAS __attribute__((address_space(3)))
; template <class AT_>
; __device__ __forceinline__ void rwkv_scan_phase(const AT_& a, Frame& F, int j) {
;     ...
;                     auto ld = [&](int t) { RwOps o; const LAS float* p = ob + t * 64 + 8 * kg;
;                         o.a0 = *(const LAS f32x4*)p; o.a1 = *(const LAS f32x4*)(p + 4); p += RW_T * 64; o.r0 = *(const LAS f32x4*)p; o.r1 = *(const LAS f32x4*)(p + 4); p += RW_T * 64;
;                         o.w0 = *(const LAS f32x4*)p; o.w1 = *(const LAS f32x4*)(p + 4); p += RW_T * 64; o.b0 = *(const LAS f32x4*)p; o.b1 = *(const LAS f32x4*)(p + 4); p += RW_T * 64;
;                         o.k0 = *(const LAS f32x4*)p; o.k1 = *(const LAS f32x4*)(p + 4);
;                         o.v = *(const LAS f32x2*)(ob + 5 * RW_T * 64 + t * 64 + v0); o.sc = *(const LAS f32x2*)(ob + 6 * RW_T * 64 + t * 4); return o; };
;                     auto step = [&](const RwOps& cur, int t) {
;                         const f32x2 a01 = {cur.a0.x, cur.a0.y}, a23 = {cur.a0.z, cur.a0.w}, a45 = {cur.a1.x, cur.a1.y}, a67 = {cur.a1.z, cur.a1.w};
;                         const f32x2 r01 = {cur.r0.x, cur.r0.y}, r23 = {cur.r0.z, cur.r0.w}, r45 = {cur.r1.x, cur.r1.y}, r67 = {cur.r1.z, cur.r1.w};
;                         f32x2 sA0 = S0[0] * a01, sA1 = S1[0] * a01, sY0 = S0[0] * r01, sY1 = S1[0] * r01;
;                         sA0 = S0[1] * a23 + sA0; sA1 = S1[1] * a23 + sA1; sY0 = S0[1] * r23 + sY0; sY1 = S1[1] * r23 + sY1;
;                         sA0 = S0[2] * a45 + sA0; sA1 = S1[2] * a45 + sA1; sY0 = S0[2] * r45 + sY0; sY1 = S1[2] * r45 + sY1;
;                         sA0 = S0[3] * a67 + sA0; sA1 = S1[3] * a67 + sA1; sY0 = S0[3] * r67 + sY0; sY1 = S1[3] * r67 + sY1;
;                         const float sa0 = row8_allsum(sA0.x + sA0.y), sa1 = row8_allsum(sA1.x + sA1.y), yy0 = row8_allsum(sY0.x + sY0.y), yy1 = row8_allsum(sY1.x + sY1.y);
;                         if (kg == 0) { f32x2 yo; yo.x = yy0 + sa0 * cur.sc.x + cur.v.x * cur.sc.y; yo.y = yy1 + sa1 * cur.sc.x + cur.v.y * cur.sc.y; *(LAS f32x2*)(Yb + t * 64 + v0) = yo; }
;                         const f32x2 w01 = {cur.w0.x, cur.w0.y}, w23 = {cur.w0.z, cur.w0.w}, w45 = {cur.w1.x, cur.w1.y}, w67 = {cur.w1.z, cur.w1.w};
;                         const f32x2 b01 = {cur.b0.x, cur.b0.y}, b23 = {cur.b0.z, cur.b0.w}, b45 = {cur.b1.x, cur.b1.y}, b67 = {cur.b1.z, cur.b1.w};
	ds_read_b128 v[2:5], v50 offset:1280
	ds_read_b128 v[6:9], v50 offset:1296
	ds_read_b128 v[10:13], v50 offset:9472
	ds_read_b128 v[14:17], v50 offset:9488
	ds_read_b128 v[18:21], v50 offset:17664
	ds_read_b128 v[22:25], v50 offset:17680
	ds_read_b128 v[26:29], v50 offset:25856
	ds_read_b128 v[30:33], v50 offset:25872
	ds_read_b128 v[34:37], v50 offset:34048
	ds_read_b128 v[38:41], v50 offset:34064
	ds_read2_b64 v[220:223], v51 offset0:128 offset1:160
	ds_read2_b64 v[224:227], v52 offset0:8 offset1:10
	v_pk_mul_f32 v[46:47], v[150:151], v[168:169] op_sel_hi:[1,0]
	v_pk_mul_f32 v[48:49], v[150:151], v[176:177] op_sel_hi:[1,0]
	v_pk_fma_f32 v[46:47], v[152:153], v[168:169], v[46:47] op_sel:[0,1,0]
	v_pk_fma_f32 v[48:49], v[152:153], v[176:177], v[48:49] op_sel:[0,1,0]
	v_pk_fma_f32 v[46:47], v[154:155], v[170:171], v[46:47] op_sel_hi:[1,0,1]
	v_pk_fma_f32 v[48:49], v[154:155], v[178:179], v[48:49] op_sel_hi:[1,0,1]
	v_pk_fma_f32 v[46:47], v[156:157], v[170:171], v[46:47] op_sel:[0,1,0]
	v_pk_fma_f32 v[48:49], v[156:157], v[178:179], v[48:49] op_sel:[0,1,0]
	v_pk_fma_f32 v[46:47], v[158:159], v[172:173], v[46:47] op_sel_hi:[1,0,1]
	v_pk_fma_f32 v[48:49], v[158:159], v[180:181], v[48:49] op_sel_hi:[1,0,1]
	v_pk_fma_f32 v[46:47], v[160:161], v[172:173], v[46:47] op_sel:[0,1,0]
	v_pk_fma_f32 v[48:49], v[160:161], v[180:181], v[48:49] op_sel:[0,1,0]
	v_pk_fma_f32 v[46:47], v[162:163], v[174:175], v[46:47] op_sel_hi:[1,0,1]
	v_pk_fma_f32 v[48:49], v[162:163], v[182:183], v[48:49] op_sel_hi:[1,0,1]
	v_pk_fma_f32 v[46:47], v[164:165], v[174:175], v[46:47] op_sel:[0,1,0]
	v_pk_fma_f32 v[48:49], v[164:165], v[182:183], v[48:49] op_sel:[0,1,0]
	v_pk_mul_f32 v[150:151], v[150:151], v[184:185] op_sel_hi:[1,0]
	v_pk_mul_f32 v[152:153], v[152:153], v[184:185] op_sel:[0,1]
	v_pk_mul_f32 v[154:155], v[154:155], v[186:187] op_sel_hi:[1,0]
	v_pk_mul_f32 v[156:157], v[156:157], v[186:187] op_sel:[0,1]
	v_pk_mul_f32 v[158:159], v[158:159], v[188:189] op_sel_hi:[1,0]
	v_pk_mul_f32 v[160:161], v[160:161], v[188:189] op_sel:[0,1]
	v_pk_mul_f32 v[162:163], v[162:163], v[190:191] op_sel_hi:[1,0]
	v_pk_mul_f32 v[164:165], v[164:165], v[190:191] op_sel:[0,1]
	v_add_f32_dpp v46, v46, v46 quad_perm:[1,0,3,2] row_mask:0xf bank_mask:0xf bound_ctrl:1
	v_add_f32_dpp v47, v47, v47 quad_perm:[1,0,3,2] row_mask:0xf bank_mask:0xf bound_ctrl:1
	v_add_f32_dpp v48, v48, v48 quad_perm:[1,0,3,2] row_mask:0xf bank_mask:0xf bound_ctrl:1
	v_add_f32_dpp v49, v49, v49 quad_perm:[1,0,3,2] row_mask:0xf bank_mask:0xf bound_ctrl:1
	v_add_f32_dpp v46, v46, v46 quad_perm:[2,3,0,1] row_mask:0xf bank_mask:0xf bound_ctrl:1
	v_add_f32_dpp v47, v47, v47 quad_perm:[2,3,0,1] row_mask:0xf bank_mask:0xf bound_ctrl:1
	v_add_f32_dpp v48, v48, v48 quad_perm:[2,3,0,1] row_mask:0xf bank_mask:0xf bound_ctrl:1
	v_add_f32_dpp v49, v49, v49 quad_perm:[2,3,0,1] row_mask:0xf bank_mask:0xf bound_ctrl:1
	v_add_f32_dpp v46, v46, v46 row_half_mirror row_mask:0xf bank_mask:0xf bound_ctrl:1
	v_add_f32_dpp v47, v47, v47 row_half_mirror row_mask:0xf bank_mask:0xf bound_ctrl:1
	v_add_f32_dpp v48, v48, v48 row_half_mirror row_mask:0xf bank_mask:0xf bound_ctrl:1
	v_add_f32_dpp v49, v49, v49 row_half_mirror row_mask:0xf bank_mask:0xf bound_ctrl:1
	v_pk_fma_f32 v[48:49], v[46:47], v[216:217], v[48:49] op_sel_hi:[1,0,1]
	v_pk_fma_f32 v[48:49], v[212:213], v[216:217], v[48:49] op_sel:[0,1,0]
	s_mov_b64 exec, s[100:101]
	ds_write_b64 v53, v[48:49] offset:1024
	s_mov_b64 exec, -1
	v_pk_fma_f32 v[150:151], v[46:47], v[192:193], v[150:151] op_sel_hi:[1,0,1]
	v_pk_fma_f32 v[152:153], v[46:47], v[192:193], v[152:153] op_sel:[0,1,0]
	v_pk_fma_f32 v[154:155], v[46:47], v[194:195], v[154:155] op_sel_hi:[1,0,1]
	v_pk_fma_f32 v[156:157], v[46:47], v[194:195], v[156:157] op_sel:[0,1,0]
	v_pk_fma_f32 v[158:159], v[46:47], v[196:197], v[158:159] op_sel_hi:[1,0,1]
	v_pk_fma_f32 v[160:161], v[46:47], v[196:197], v[160:161] op_sel:[0,1,0]
	v_pk_fma_f32 v[162:163], v[46:47], v[198:199], v[162:163] op_sel_hi:[1,0,1]
	v_pk_fma_f32 v[164:165], v[46:47], v[198:199], v[164:165] op_sel:[0,1,0]
	v_pk_fma_f32 v[150:151], v[212:213], v[200:201], v[150:151] op_sel_hi:[1,0,1]
	v_pk_fma_f32 v[152:153], v[212:213], v[200:201], v[152:153] op_sel:[0,1,0]
	v_pk_fma_f32 v[154:155], v[212:213], v[202:203], v[154:155] op_sel_hi:[1,0,1]
	v_pk_fma_f32 v[156:157], v[212:213], v[202:203], v[156:157] op_sel:[0,1,0]
	v_pk_fma_f32 v[158:159], v[212:213], v[204:205], v[158:159] op_sel_hi:[1,0,1]
	v_pk_fma_f32 v[160:161], v[212:213], v[204:205], v[160:161] op_sel:[0,1,0]
	v_pk_fma_f32 v[162:163], v[212:213], v[206:207], v[162:163] op_sel_hi:[1,0,1]
	v_pk_fma_f32 v[164:165], v[212:213], v[206:207], v[164:165] op_sel:[0,1,0]
	s_waitcnt lgkmcnt(0)
; #define LAS __attribute__((address_space(3)))
; template <class AT_>
; __device__ __forceinline__ void rwkv_scan_phase(const AT_& a, Frame& F, int j) {
;     ...
;                     auto ld = [&](int t) { RwOps o; const LAS float* p = ob + t * 64 + 8 * kg;
;                         o.a0 = *(const LAS f32x4*)p; o.a1 = *(const LAS f32x4*)(p + 4); p += RW_T * 64; o.r0 = *(const LAS f32x4*)p; o.r1 = *(const LAS f32x4*)(p + 4); p += RW_T * 64;
;                         o.w0 = *(const LAS f32x4*)p; o.w1 = *(const LAS f32x4*)(p + 4); p += RW_T * 64; o.b0 = *(const LAS f32x4*)p; o.b1 = *(const LAS f32x4*)(p + 4); p += RW_T * 64;
;                         o.k0 = *(const LAS f32x4*)p; o.k1 = *(const LAS f32x4*)(p + 4);
;                         o.v = *(const LAS f32x2*)(ob + 5 * RW_T * 64 + t * 64 + v0); o.sc = *(const LAS f32x2*)(ob + 6 * RW_T * 64 + t * 4); return o; };
;                     auto step = [&](const RwOps& cur, int t) {
;                         const f32x2 a01 = {cur.a0.x, cur.a0.y}, a23 = {cur.a0.z, cur.a0.w}, a45 = {cur.a1.x, cur.a1.y}, a67 = {cur.a1.z, cur.a1.w};
;                         const f32x2 r01 = {cur.r0.x, cur.r0.y}, r23 = {cur.r0.z, cur.r0.w}, r45 = {cur.r1.x, cur.r1.y}, r67 = {cur.r1.z, cur.r1.w};
;                         f32x2 sA0 = S0[0] * a01, sA1 = S1[0] * a01, sY0 = S0[0] * r01, sY1 = S1[0] * r01;
;                         sA0 = S0[1] * a23 + sA0; sA1 = S1[1] * a23 + sA1; sY0 = S0[1] * r23 + sY0; sY1 = S1[1] * r23 + sY1;
;                         sA0 = S0[2] * a45 + sA0; sA1 = S1[2] * a45 + sA1; sY0 = S0[2] * r45 + sY0; sY1 = S1[2] * r45 + sY1;
;                         sA0 = S0[3] * a67 + sA0; sA1 = S1[3] * a67 + sA1; sY0 = S0[3] * r67 + sY0; sY1 = S1[3] * r67 + sY1;
;                         const float sa0 = row8_allsum(sA0.x + sA0.y), sa1 = row8_allsum(sA1.x + sA1.y), yy0 = row8_allsum(sY0.x + sY0.y), yy1 = row8_allsum(sY1.x + sY1.y);
;                         if (kg == 0) { f32x2 yo; yo.x = yy0 + sa0 * cur.sc.x + cur.v.x * cur.sc.y; yo.y = yy1 + sa1 * cur.sc.x + cur.v.y * cur.sc.y; *(LAS f32x2*)(Yb + t * 64 + v0) = yo; }
;                         const f32x2 w01 = {cur.w0.x, cur.w0.y}, w23 = {cur.w0.z, cur.w0.w}, w45 = {cur.w1.x, cur.w1.y}, w67 = {cur.w1.z, cur.w1.w};
;                         const f32x2 b01 = {cur.b0.x, cur.b0.y}, b23 = {cur.b0.z, cur.b0.w}, b45 = {cur.b1.x, cur.b1.y}, b67 = {cur.b1.z, cur.b1.w};
	ds_read_b128 v[168:171], v50 offset:1536
	ds_read_b128 v[172:175], v50 offset:1552
	ds_read_b128 v[176:179], v50 offset:9728
	ds_read_b128 v[180:183], v50 offset:9744
	ds_read_b128 v[184:187], v50 offset:17920
	ds_read_b128 v[188:191], v50 offset:17936
	ds_read_b128 v[192:195], v50 offset:26112
	ds_read_b128 v[196:199], v50 offset:26128
	ds_read_b128 v[200:203], v50 offset:34304
	ds_read_b128 v[204:207], v50 offset:34320
	v_pk_mul_f32 v[46:47], v[150:151], v[2:3] op_sel_hi:[1,0]
	v_pk_mul_f32 v[48:49], v[150:151], v[10:11] op_sel_hi:[1,0]
	v_pk_fma_f32 v[46:47], v[152:153], v[2:3], v[46:47] op_sel:[0,1,0]
	v_pk_fma_f32 v[48:49], v[152:153], v[10:11], v[48:49] op_sel:[0,1,0]
	v_pk_fma_f32 v[46:47], v[154:155], v[4:5], v[46:47] op_sel_hi:[1,0,1]
	v_pk_fma_f32 v[48:49], v[154:155], v[12:13], v[48:49] op_sel_hi:[1,0,1]
	v_pk_fma_f32 v[46:47], v[156:157], v[4:5], v[46:47] op_sel:[0,1,0]
	v_pk_fma_f32 v[48:49], v[156:157], v[12:13], v[48:49] op_sel:[0,1,0]
	v_pk_fma_f32 v[46:47], v[158:159], v[6:7], v[46:47] op_sel_hi:[1,0,1]
	v_pk_fma_f32 v[48:49], v[158:159], v[14:15], v[48:49] op_sel_hi:[1,0,1]
	v_pk_fma_f32 v[46:47], v[160:161], v[6:7], v[46:47] op_sel:[0,1,0]
	v_pk_fma_f32 v[48:49], v[160:161], v[14:15], v[48:49] op_sel:[0,1,0]
	v_pk_fma_f32 v[46:47], v[162:163], v[8:9], v[46:47] op_sel_hi:[1,0,1]
	v_pk_fma_f32 v[48:49], v[162:163], v[16:17], v[48:49] op_sel_hi:[1,0,1]
	v_pk_fma_f32 v[46:47], v[164:165], v[8:9], v[46:47] op_sel:[0,1,0]
	v_pk_fma_f32 v[48:49], v[164:165], v[16:17], v[48:49] op_sel:[0,1,0]
	v_pk_mul_f32 v[150:151], v[150:151], v[18:19] op_sel_hi:[1,0]
	v_pk_mul_f32 v[152:153], v[152:153], v[18:19] op_sel:[0,1]
	v_pk_mul_f32 v[154:155], v[154:155], v[20:21] op_sel_hi:[1,0]
	v_pk_mul_f32 v[156:157], v[156:157], v[20:21] op_sel:[0,1]
	v_pk_mul_f32 v[158:159], v[158:159], v[22:23] op_sel_hi:[1,0]
	v_pk_mul_f32 v[160:161], v[160:161], v[22:23] op_sel:[0,1]
	v_pk_mul_f32 v[162:163], v[162:163], v[24:25] op_sel_hi:[1,0]
	v_pk_mul_f32 v[164:165], v[164:165], v[24:25] op_sel:[0,1]
	v_add_f32_dpp v46, v46, v46 quad_perm:[1,0,3,2] row_mask:0xf bank_mask:0xf bound_ctrl:1
	v_add_f32_dpp v47, v47, v47 quad_perm:[1,0,3,2] row_mask:0xf bank_mask:0xf bound_ctrl:1
	v_add_f32_dpp v48, v48, v48 quad_perm:[1,0,3,2] row_mask:0xf bank_mask:0xf bound_ctrl:1
	v_add_f32_dpp v49, v49, v49 quad_perm:[1,0,3,2] row_mask:0xf bank_mask:0xf bound_ctrl:1
	v_add_f32_dpp v46, v46, v46 quad_perm:[2,3,0,1] row_mask:0xf bank_mask:0xf bound_ctrl:1
	v_add_f32_dpp v47, v47, v47 quad_perm:[2,3,0,1] row_mask:0xf bank_mask:0xf bound_ctrl:1
	v_add_f32_dpp v48, v48, v48 quad_perm:[2,3,0,1] row_mask:0xf bank_mask:0xf bound_ctrl:1
	v_add_f32_dpp v49, v49, v49 quad_perm:[2,3,0,1] row_mask:0xf bank_mask:0xf bound_ctrl:1
	v_add_f32_dpp v46, v46, v46 row_half_mirror row_mask:0xf bank_mask:0xf bound_ctrl:1
	v_add_f32_dpp v47, v47, v47 row_half_mirror row_mask:0xf bank_mask:0xf bound_ctrl:1
	v_add_f32_dpp v48, v48, v48 row_half_mirror row_mask:0xf bank_mask:0xf bound_ctrl:1
	v_add_f32_dpp v49, v49, v49 row_half_mirror row_mask:0xf bank_mask:0xf bound_ctrl:1
	v_pk_fma_f32 v[48:49], v[46:47], v[218:219], v[48:49] op_sel_hi:[1,0,1]
	v_pk_fma_f32 v[48:49], v[214:215], v[218:219], v[48:49] op_sel:[0,1,0]
	s_mov_b64 exec, s[100:101]
	ds_write_b64 v53, v[48:49] offset:1280
	s_mov_b64 exec, -1
	v_pk_fma_f32 v[150:151], v[46:47], v[26:27], v[150:151] op_sel_hi:[1,0,1]
	v_pk_fma_f32 v[152:153], v[46:47], v[26:27], v[152:153] op_sel:[0,1,0]
	v_pk_fma_f32 v[154:155], v[46:47], v[28:29], v[154:155] op_sel_hi:[1,0,1]
	v_pk_fma_f32 v[156:157], v[46:47], v[28:29], v[156:157] op_sel:[0,1,0]
	v_pk_fma_f32 v[158:159], v[46:47], v[30:31], v[158:159] op_sel_hi:[1,0,1]
	v_pk_fma_f32 v[160:161], v[46:47], v[30:31], v[160:161] op_sel:[0,1,0]
	v_pk_fma_f32 v[162:163], v[46:47], v[32:33], v[162:163] op_sel_hi:[1,0,1]
	v_pk_fma_f32 v[164:165], v[46:47], v[32:33], v[164:165] op_sel:[0,1,0]
	v_pk_fma_f32 v[150:151], v[214:215], v[34:35], v[150:151] op_sel_hi:[1,0,1]
	v_pk_fma_f32 v[152:153], v[214:215], v[34:35], v[152:153] op_sel:[0,1,0]
	v_pk_fma_f32 v[154:155], v[214:215], v[36:37], v[154:155] op_sel_hi:[1,0,1]
	v_pk_fma_f32 v[156:157], v[214:215], v[36:37], v[156:157] op_sel:[0,1,0]
	v_pk_fma_f32 v[158:159], v[214:215], v[38:39], v[158:159] op_sel_hi:[1,0,1]
	v_pk_fma_f32 v[160:161], v[214:215], v[38:39], v[160:161] op_sel:[0,1,0]
	v_pk_fma_f32 v[162:163], v[214:215], v[40:41], v[162:163] op_sel_hi:[1,0,1]
	v_pk_fma_f32 v[164:165], v[214:215], v[40:41], v[164:165] op_sel:[0,1,0]
	s_waitcnt lgkmcnt(0)
; #define LAS __attribute__((address_space(3)))
; template <class AT_>
; __device__ __forceinline__ void rwkv_scan_phase(const AT_& a, Frame& F, int j) {
;     ...
;                     auto ld = [&](int t) { RwOps o; const LAS float* p = ob + t * 64 + 8 * kg;
;                         o.a0 = *(const LAS f32x4*)p; o.a1 = *(const LAS f32x4*)(p + 4); p += RW_T * 64; o.r0 = *(const LAS f32x4*)p; o.r1 = *(const LAS f32x4*)(p + 4); p += RW_T * 64;
;                         o.w0 = *(const LAS f32x4*)p; o.w1 = *(const LAS f32x4*)(p + 4); p += RW_T * 64; o.b0 = *(const LAS f32x4*)p; o.b1 = *(const LAS f32x4*)(p + 4); p += RW_T * 64;
;                         o.k0 = *(const LAS f32x4*)p; o.k1 = *(const LAS f32x4*)(p + 4);
;                         o.v = *(const LAS f32x2*)(ob + 5 * RW_T * 64 + t * 64 + v0); o.sc = *(const LAS f32x2*)(ob + 6 * RW_T * 64 + t * 4); return o; };
;                     auto step = [&](const RwOps& cur, int t) {
;                         const f32x2 a01 = {cur.a0.x, cur.a0.y}, a23 = {cur.a0.z, cur.a0.w}, a45 = {cur.a1.x, cur.a1.y}, a67 = {cur.a1.z, cur.a1.w};
;                         const f32x2 r01 = {cur.r0.x, cur.r0.y}, r23 = {cur.r0.z, cur.r0.w}, r45 = {cur.r1.x, cur.r1.y}, r67 = {cur.r1.z, cur.r1.w};
;                         f32x2 sA0 = S0[0] * a01, sA1 = S1[0] * a01, sY0 = S0[0] * r01, sY1 = S1[0] * r01;
;                         sA0 = S0[1] * a23 + sA0; sA1 = S1[1] * a23 + sA1; sY0 = S0[1] * r23 + sY0; sY1 = S1[1] * r23 + sY1;
;                         sA0 = S0[2] * a45 + sA0; sA1 = S1[2] * a45 + sA1; sY0 = S0[2] * r45 + sY0; sY1 = S1[2] * r45 + sY1;
;                         sA0 = S0[3] * a67 + sA0; sA1 = S1[3] * a67 + sA1; sY0 = S0[3] * r67 + sY0; sY1 = S1[3] * r67 + sY1;
;                         const float sa0 = row8_allsum(sA0.x + sA0.y), sa1 = row8_allsum(sA1.x + sA1.y), yy0 = row8_allsum(sY0.x + sY0.y), yy1 = row8_allsum(sY1.x + sY1.y);
;                         if (kg == 0) { f32x2 yo; yo.x = yy0 + sa0 * cur.sc.x + cur.v.x * cur.sc.y; yo.y = yy1 + sa1 * cur.sc.x + cur.v.y * cur.sc.y; *(LAS f32x2*)(Yb + t * 64 + v0) = yo; }
;                         const f32x2 w01 = {cur.w0.x, cur.w0.y}, w23 = {cur.w0.z, cur.w0.w}, w45 = {cur.w1.x, cur.w1.y}, w67 = {cur.w1.z, cur.w1.w};
;                         const f32x2 b01 = {cur.b0.x, cur.b0.y}, b23 = {cur.b0.z, cur.b0.w}, b45 = {cur.b1.x, cur.b1.y}, b67 = {cur.b1.z, cur.b1.w};
	ds_read_b128 v[2:5], v50 offset:1792
	ds_read_b128 v[6:9], v50 offset:1808
	ds_read_b128 v[10:13], v50 offset:9984
	ds_read_b128 v[14:17], v50 offset:10000
	ds_read_b128 v[18:21], v50 offset:18176
	ds_read_b128 v[22:25], v50 offset:18192
	ds_read_b128 v[26:29], v50 offset:26368
	ds_read_b128 v[30:33], v50 offset:26384
	ds_read_b128 v[34:37], v50 offset:34560
	ds_read_b128 v[38:41], v50 offset:34576
	ds_read2_b64 v[212:215], v51 offset0:192 offset1:224
	ds_read2_b64 v[216:219], v52 offset0:12 offset1:14
	v_pk_mul_f32 v[46:47], v[150:151], v[168:169] op_sel_hi:[1,0]
	v_pk_mul_f32 v[48:49], v[150:151], v[176:177] op_sel_hi:[1,0]
	v_pk_fma_f32 v[46:47], v[152:153], v[168:169], v[46:47] op_sel:[0,1,0]
	v_pk_fma_f32 v[48:49], v[152:153], v[176:177], v[48:49] op_sel:[0,1,0]
	v_pk_fma_f32 v[46:47], v[154:155], v[170:171], v[46:47] op_sel_hi:[1,0,1]
	v_pk_fma_f32 v[48:49], v[154:155], v[178:179], v[48:49] op_sel_hi:[1,0,1]
	v_pk_fma_f32 v[46:47], v[156:157], v[170:171], v[46:47] op_sel:[0,1,0]
	v_pk_fma_f32 v[48:49], v[156:157], v[178:179], v[48:49] op_sel:[0,1,0]
	v_pk_fma_f32 v[46:47], v[158:159], v[172:173], v[46:47] op_sel_hi:[1,0,1]
	v_pk_fma_f32 v[48:49], v[158:159], v[180:181], v[48:49] op_sel_hi:[1,0,1]
	v_pk_fma_f32 v[46:47], v[160:161], v[172:173], v[46:47] op_sel:[0,1,0]
	v_pk_fma_f32 v[48:49], v[160:161], v[180:181], v[48:49] op_sel:[0,1,0]
	v_pk_fma_f32 v[46:47], v[162:163], v[174:175], v[46:47] op_sel_hi:[1,0,1]
	v_pk_fma_f32 v[48:49], v[162:163], v[182:183], v[48:49] op_sel_hi:[1,0,1]
	v_pk_fma_f32 v[46:47], v[164:165], v[174:175], v[46:47] op_sel:[0,1,0]
	v_pk_fma_f32 v[48:49], v[164:165], v[182:183], v[48:49] op_sel:[0,1,0]
	v_pk_mul_f32 v[150:151], v[150:151], v[184:185] op_sel_hi:[1,0]
	v_pk_mul_f32 v[152:153], v[152:153], v[184:185] op_sel:[0,1]
	v_pk_mul_f32 v[154:155], v[154:155], v[186:187] op_sel_hi:[1,0]
	v_pk_mul_f32 v[156:157], v[156:157], v[186:187] op_sel:[0,1]
	v_pk_mul_f32 v[158:159], v[158:159], v[188:189] op_sel_hi:[1,0]
	v_pk_mul_f32 v[160:161], v[160:161], v[188:189] op_sel:[0,1]
	v_pk_mul_f32 v[162:163], v[162:163], v[190:191] op_sel_hi:[1,0]
	v_pk_mul_f32 v[164:165], v[164:165], v[190:191] op_sel:[0,1]
	v_add_f32_dpp v46, v46, v46 quad_perm:[1,0,3,2] row_mask:0xf bank_mask:0xf bound_ctrl:1
	v_add_f32_dpp v47, v47, v47 quad_perm:[1,0,3,2] row_mask:0xf bank_mask:0xf bound_ctrl:1
	v_add_f32_dpp v48, v48, v48 quad_perm:[1,0,3,2] row_mask:0xf bank_mask:0xf bound_ctrl:1
	v_add_f32_dpp v49, v49, v49 quad_perm:[1,0,3,2] row_mask:0xf bank_mask:0xf bound_ctrl:1
	v_add_f32_dpp v46, v46, v46 quad_perm:[2,3,0,1] row_mask:0xf bank_mask:0xf bound_ctrl:1
	v_add_f32_dpp v47, v47, v47 quad_perm:[2,3,0,1] row_mask:0xf bank_mask:0xf bound_ctrl:1
	v_add_f32_dpp v48, v48, v48 quad_perm:[2,3,0,1] row_mask:0xf bank_mask:0xf bound_ctrl:1
	v_add_f32_dpp v49, v49, v49 quad_perm:[2,3,0,1] row_mask:0xf bank_mask:0xf bound_ctrl:1
	v_add_f32_dpp v46, v46, v46 row_half_mirror row_mask:0xf bank_mask:0xf bound_ctrl:1
	v_add_f32_dpp v47, v47, v47 row_half_mirror row_mask:0xf bank_mask:0xf bound_ctrl:1
	v_add_f32_dpp v48, v48, v48 row_half_mirror row_mask:0xf bank_mask:0xf bound_ctrl:1
	v_add_f32_dpp v49, v49, v49 row_half_mirror row_mask:0xf bank_mask:0xf bound_ctrl:1
	v_pk_fma_f32 v[48:49], v[46:47], v[224:225], v[48:49] op_sel_hi:[1,0,1]
	v_pk_fma_f32 v[48:49], v[220:221], v[224:225], v[48:49] op_sel:[0,1,0]
	s_mov_b64 exec, s[100:101]
	ds_write_b64 v53, v[48:49] offset:1536
	s_mov_b64 exec, -1
	v_pk_fma_f32 v[150:151], v[46:47], v[192:193], v[150:151] op_sel_hi:[1,0,1]
	v_pk_fma_f32 v[152:153], v[46:47], v[192:193], v[152:153] op_sel:[0,1,0]
	v_pk_fma_f32 v[154:155], v[46:47], v[194:195], v[154:155] op_sel_hi:[1,0,1]
	v_pk_fma_f32 v[156:157], v[46:47], v[194:195], v[156:157] op_sel:[0,1,0]
	v_pk_fma_f32 v[158:159], v[46:47], v[196:197], v[158:159] op_sel_hi:[1,0,1]
	v_pk_fma_f32 v[160:161], v[46:47], v[196:197], v[160:161] op_sel:[0,1,0]
	v_pk_fma_f32 v[162:163], v[46:47], v[198:199], v[162:163] op_sel_hi:[1,0,1]
	v_pk_fma_f32 v[164:165], v[46:47], v[198:199], v[164:165] op_sel:[0,1,0]
	v_pk_fma_f32 v[150:151], v[220:221], v[200:201], v[150:151] op_sel_hi:[1,0,1]
	v_pk_fma_f32 v[152:153], v[220:221], v[200:201], v[152:153] op_sel:[0,1,0]
	v_pk_fma_f32 v[154:155], v[220:221], v[202:203], v[154:155] op_sel_hi:[1,0,1]
	v_pk_fma_f32 v[156:157], v[220:221], v[202:203], v[156:157] op_sel:[0,1,0]
	v_pk_fma_f32 v[158:159], v[220:221], v[204:205], v[158:159] op_sel_hi:[1,0,1]
	v_pk_fma_f32 v[160:161], v[220:221], v[204:205], v[160:161] op_sel:[0,1,0]
	v_pk_fma_f32 v[162:163], v[220:221], v[206:207], v[162:163] op_sel_hi:[1,0,1]
	v_pk_fma_f32 v[164:165], v[220:221], v[206:207], v[164:165] op_sel:[0,1,0]
	s_waitcnt lgkmcnt(0)
; template <class AT_>
; __device__ __forceinline__ void rwkv_scan_phase(const AT_& a, Frame& F, int j) {
;     ...
;                     auto step = [&](const RwOps& cur, int t) {
;                         const f32x2 a01 = {cur.a0.x, cur.a0.y}, a23 = {cur.a0.z, cur.a0.w}, a45 = {cur.a1.x, cur.a1.y}, a67 = {cur.a1.z, cur.a1.w};
;                         const f32x2 r01 = {cur.r0.x, cur.r0.y}, r23 = {cur.r0.z, cur.r0.w}, r45 = {cur.r1.x, cur.r1.y}, r67 = {cur.r1.z, cur.r1.w};
;                         f32x2 sA0 = S0[0] * a01, sA1 = S1[0] * a01, sY0 = S0[0] * r01, sY1 = S1[0] * r01;
;                         sA0 = S0[1] * a23 + sA0; sA1 = S1[1] * a23 + sA1; sY0 = S0[1] * r23 + sY0; sY1 = S1[1] * r23 + sY1;
;                         sA0 = S0[2] * a45 + sA0; sA1 = S1[2] * a45 + sA1; sY0 = S0[2] * r45 + sY0; sY1 = S1[2] * r45 + sY1;
;                         sA0 = S0[3] * a67 + sA0; sA1 = S1[3] * a67 + sA1; sY0 = S0[3] * r67 + sY0; sY1 = S1[3] * r67 + sY1;
;                         const float sa0 = row8_allsum(sA0.x + sA0.y), sa1 = row8_allsum(sA1.x + sA1.y), yy0 = row8_allsum(sY0.x + sY0.y), yy1 = row8_allsum(sY1.x + sY1.y);
;                         if (kg == 0) { f32x2 yo; yo.x = yy0 + sa0 * cur.sc.x + cur.v.x * cur.sc.y; yo.y = yy1 + sa1 * cur.sc.x + cur.v.y * cur.sc.y; *(LAS f32x2*)(Yb + t * 64 + v0) = yo; }
;                         const f32x2 w01 = {cur.w0.x, cur.w0.y}, w23 = {cur.w0.z, cur.w0.w}, w45 = {cur.w1.x, cur.w1.y}, w67 = {cur.w1.z, cur.w1.w};
;                         const f32x2 b01 = {cur.b0.x, cur.b0.y}, b23 = {cur.b0.z, cur.b0.w}, b45 = {cur.b1.x, cur.b1.y}, b67 = {cur.b1.z, cur.b1.w};
;                         const f32x2 k01 = {cur.k0.x, cur.k0.y}, k23 = {cur.k0.z, cur.k0.w}, k45 = {cur.k1.x, cur.k1.y}, k67 = {cur.k1.z, cur.k1.w};
;                         const f32x2 s0 = {sa0, sa0}, s1 = {sa1, sa1}, x0 = {cur.v.x, cur.v.x}, x1 = {cur.v.y, cur.v.y};
;                         S0[0] = S0[0] * w01 + (s0 * b01 + x0 * k01); S0[1] = S0[1] * w23 + (s0 * b23 + x0 * k23); S0[2] = S0[2] * w45 + (s0 * b45 + x0 * k45); S0[3] = S0[3] * w67 + (s0 * b67 + x0 * k67);
;                         S1[0] = S1[0] * w01 + (s1 * b01 + x1 * k01); S1[1] = S1[1] * w23 + (s1 * b23 + x1 * k23); S1[2] = S1[2] * w45 + (s1 * b45 + x1 * k45); S1[3] = S1[3] * w67 + (s1 * b67 + x1 * k67);
;                     };
;                     RwOps oa = ld(0);
	ds_read_b128 v[168:171], v50 offset:2048
	ds_read_b128 v[172:175], v50 offset:2064
	ds_read_b128 v[176:179], v50 offset:10240
	ds_read_b128 v[180:183], v50 offset:10256
	ds_read_b128 v[184:187], v50 offset:18432
	ds_read_b128 v[188:191], v50 offset:18448
	ds_read_b128 v[192:195], v50 offset:26624
	ds_read_b128 v[196:199], v50 offset:26640
	ds_read_b128 v[200:203], v50 offset:34816
	ds_read_b128 v[204:207], v50 offset:34832
	v_pk_mul_f32 v[46:47], v[150:151], v[2:3] op_sel_hi:[1,0]
	v_pk_mul_f32 v[48:49], v[150:151], v[10:11] op_sel_hi:[1,0]
	v_pk_fma_f32 v[46:47], v[152:153], v[2:3], v[46:47] op_sel:[0,1,0]
	v_pk_fma_f32 v[48:49], v[152:153], v[10:11], v[48:49] op_sel:[0,1,0]
	v_pk_fma_f32 v[46:47], v[154:155], v[4:5], v[46:47] op_sel_hi:[1,0,1]
	v_pk_fma_f32 v[48:49], v[154:155], v[12:13], v[48:49] op_sel_hi:[1,0,1]
	v_pk_fma_f32 v[46:47], v[156:157], v[4:5], v[46:47] op_sel:[0,1,0]
	v_pk_fma_f32 v[48:49], v[156:157], v[12:13], v[48:49] op_sel:[0,1,0]
	v_pk_fma_f32 v[46:47], v[158:159], v[6:7], v[46:47] op_sel_hi:[1,0,1]
	v_pk_fma_f32 v[48:49], v[158:159], v[14:15], v[48:49] op_sel_hi:[1,0,1]
	v_pk_fma_f32 v[46:47], v[160:161], v[6:7], v[46:47] op_sel:[0,1,0]
	v_pk_fma_f32 v[48:49], v[160:161], v[14:15], v[48:49] op_sel:[0,1,0]
	v_pk_fma_f32 v[46:47], v[162:163], v[8:9], v[46:47] op_sel_hi:[1,0,1]
	v_pk_fma_f32 v[48:49], v[162:163], v[16:17], v[48:49] op_sel_hi:[1,0,1]
	v_pk_fma_f32 v[46:47], v[164:165], v[8:9], v[46:47] op_sel:[0,1,0]
	v_pk_fma_f32 v[48:49], v[164:165], v[16:17], v[48:49] op_sel:[0,1,0]
	v_pk_mul_f32 v[150:151], v[150:151], v[18:19] op_sel_hi:[1,0]
	v_pk_mul_f32 v[152:153], v[152:153], v[18:19] op_sel:[0,1]
	v_pk_mul_f32 v[154:155], v[154:155], v[20:21] op_sel_hi:[1,0]
	v_pk_mul_f32 v[156:157], v[156:157], v[20:21] op_sel:[0,1]
	v_pk_mul_f32 v[158:159], v[158:159], v[22:23] op_sel_hi:[1,0]
	v_pk_mul_f32 v[160:161], v[160:161], v[22:23] op_sel:[0,1]
	v_pk_mul_f32 v[162:163], v[162:163], v[24:25] op_sel_hi:[1,0]
	v_pk_mul_f32 v[164:165], v[164:165], v[24:25] op_sel:[0,1]
	v_add_f32_dpp v46, v46, v46 quad_perm:[1,0,3,2] row_mask:0xf bank_mask:0xf bound_ctrl:1
	v_add_f32_dpp v47, v47, v47 quad_perm:[1,0,3,2] row_mask:0xf bank_mask:0xf bound_ctrl:1
	v_add_f32_dpp v48, v48, v48 quad_perm:[1,0,3,2] row_mask:0xf bank_mask:0xf bound_ctrl:1
	v_add_f32_dpp v49, v49, v49 quad_perm:[1,0,3,2] row_mask:0xf bank_mask:0xf bound_ctrl:1
	v_add_f32_dpp v46, v46, v46 quad_perm:[2,3,0,1] row_mask:0xf bank_mask:0xf bound_ctrl:1
	v_add_f32_dpp v47, v47, v47 quad_perm:[2,3,0,1] row_mask:0xf bank_mask:0xf bound_ctrl:1
	v_add_f32_dpp v48, v48, v48 quad_perm:[2,3,0,1] row_mask:0xf bank_mask:0xf bound_ctrl:1
	v_add_f32_dpp v49, v49, v49 quad_perm:[2,3,0,1] row_mask:0xf bank_mask:0xf bound_ctrl:1
	v_add_f32_dpp v46, v46, v46 row_half_mirror row_mask:0xf bank_mask:0xf bound_ctrl:1
	v_add_f32_dpp v47, v47, v47 row_half_mirror row_mask:0xf bank_mask:0xf bound_ctrl:1
	v_add_f32_dpp v48, v48, v48 row_half_mirror row_mask:0xf bank_mask:0xf bound_ctrl:1
	v_add_f32_dpp v49, v49, v49 row_half_mirror row_mask:0xf bank_mask:0xf bound_ctrl:1
	v_pk_fma_f32 v[48:49], v[46:47], v[226:227], v[48:49] op_sel_hi:[1,0,1]
	v_pk_fma_f32 v[48:49], v[222:223], v[226:227], v[48:49] op_sel:[0,1,0]
	s_mov_b64 exec, s[100:101]
	ds_write_b64 v53, v[48:49] offset:1792
	s_mov_b64 exec, -1
	v_pk_fma_f32 v[150:151], v[46:47], v[26:27], v[150:151] op_sel_hi:[1,0,1]
	v_pk_fma_f32 v[152:153], v[46:47], v[26:27], v[152:153] op_sel:[0,1,0]
	v_pk_fma_f32 v[154:155], v[46:47], v[28:29], v[154:155] op_sel_hi:[1,0,1]
	v_pk_fma_f32 v[156:157], v[46:47], v[28:29], v[156:157] op_sel:[0,1,0]
	v_pk_fma_f32 v[158:159], v[46:47], v[30:31], v[158:159] op_sel_hi:[1,0,1]
	v_pk_fma_f32 v[160:161], v[46:47], v[30:31], v[160:161] op_sel:[0,1,0]
	v_pk_fma_f32 v[162:163], v[46:47], v[32:33], v[162:163] op_sel_hi:[1,0,1]
	v_pk_fma_f32 v[164:165], v[46:47], v[32:33], v[164:165] op_sel:[0,1,0]
	v_pk_fma_f32 v[150:151], v[222:223], v[34:35], v[150:151] op_sel_hi:[1,0,1]
	v_pk_fma_f32 v[152:153], v[222:223], v[34:35], v[152:153] op_sel:[0,1,0]
	v_pk_fma_f32 v[154:155], v[222:223], v[36:37], v[154:155] op_sel_hi:[1,0,1]
	v_pk_fma_f32 v[156:157], v[222:223], v[36:37], v[156:157] op_sel:[0,1,0]
	v_pk_fma_f32 v[158:159], v[222:223], v[38:39], v[158:159] op_sel_hi:[1,0,1]
	v_pk_fma_f32 v[160:161], v[222:223], v[38:39], v[160:161] op_sel:[0,1,0]
	v_pk_fma_f32 v[162:163], v[222:223], v[40:41], v[162:163] op_sel_hi:[1,0,1]
	v_pk_fma_f32 v[164:165], v[222:223], v[40:41], v[164:165] op_sel:[0,1,0]
	v_add_u32_e32 v50, 2048, v50
	v_add_u32_e32 v51, 2048, v51
	v_add_u32_e32 v52, 128, v52
	v_add_u32_e32 v53, 2048, v53
	s_sub_u32 s98, s98, 1
	s_cmp_lg_u32 s98, 0
	s_cbranch_scc1 .Lscan_a_loop
	s_branch .LBB0_3487

; __device__ __forceinline__ void xcd_barrier(const XcdBarrier& b) {
;     asm volatile("s_waitcnt vmcnt(0)" ::: "memory");
;     __syncthreads();
;     if (threadIdx.x == 0) {
;         unsigned* bar = b.bar;
;         __builtin_amdgcn_s_waitcnt(0);
;         unsigned nloc = b.st[0], nx = b.st[1];
;         if (nloc == 0u) { xcd_barrier_complete(bar, b.x, nloc, nx); b.st[0] = nloc; b.st[1] = nx; }
.LBB0_3803:
	v_readlane_b32 s7, v247, 8
	s_cmp_lt_i32 s7, 39
	s_branch .LBB0_3849
	v_readlane_b32 s34, v247, 2
	v_readlane_b32 s35, v247, 3
	s_waitcnt vmcnt(0)
	s_barrier
	s_mov_b64 s[30:31], exec
	v_readlane_b32 s0, v247, 5
	v_readlane_b32 s1, v247, 6
	s_and_b64 s[0:1], s[30:31], s[0:1]
	s_mov_b64 exec, s[0:1]
	s_cbranch_execz .LBB0_3848
	s_add_i32 s0, 0, 0x20160
	v_mov_b32_e32 v1, s0
	s_waitcnt vmcnt(0) expcnt(0) lgkmcnt(0)
	ds_read_b32 v4, v1
	s_add_i32 s0, 0, 0x20164
	v_mov_b32_e32 v1, s0
	ds_read_b32 v2, v1
	s_waitcnt lgkmcnt(1)
	v_cmp_ne_u32_e32 vcc, 0, v4
	s_cbranch_vccnz .LBB0_3819
	s_add_u32 s2, s34, 0x1000
	s_addc_u32 s3, s35, 0
	s_load_dwordx2 s[0:1], s[4:5], 0x4
	s_add_u32 s4, s34, 0x1100
	s_addc_u32 s5, s35, 0
	s_add_u32 s6, s34, 0x1200
	s_addc_u32 s7, s35, 0
	s_add_u32 s8, s34, 0x1300
	s_waitcnt lgkmcnt(0)
	s_mul_i32 s18, s0, s33
	s_addc_u32 s9, s35, 0
	s_mul_i32 s18, s18, s1
	s_mov_b32 s19, 1
	s_mov_b64 s[0:1], 0
	v_mov_b64_e32 v[2:3], s[34:35]
	v_mov_b64_e32 v[4:5], s[2:3]
	v_mov_b64_e32 v[6:7], s[4:5]
	v_mov_b64_e32 v[8:9], s[6:7]
	v_mov_b64_e32 v[10:11], s[8:9]
	s_branch .LBB0_3809

; __device__ __forceinline__ void xcd_barrier(const XcdBarrier& b) {
;     asm volatile("s_waitcnt vmcnt(0)" ::: "memory");
;     __syncthreads();
;     if (threadIdx.x == 0) {
;         unsigned* bar = b.bar;
;         __builtin_amdgcn_s_waitcnt(0);
;         unsigned nloc = b.st[0], nx = b.st[1];
;         if (nloc == 0u) { xcd_barrier_complete(bar, b.x, nloc, nx); b.st[0] = nloc; b.st[1] = nx; }
.LBB0_4015:
	v_readlane_b32 s7, v247, 8
	s_cmp_lt_i32 s7, 41
	s_branch .LBB0_4061
	v_readlane_b32 s34, v247, 2
	v_readlane_b32 s35, v247, 3
	s_waitcnt vmcnt(0)
	s_barrier
	s_mov_b64 s[30:31], exec
	v_readlane_b32 s0, v247, 5
	v_readlane_b32 s1, v247, 6
	s_and_b64 s[0:1], s[30:31], s[0:1]
	s_mov_b64 exec, s[0:1]
	s_cbranch_execz .LBB0_4060
	s_add_i32 s0, 0, 0x20160
	v_mov_b32_e32 v1, s0
	s_waitcnt vmcnt(0) expcnt(0) lgkmcnt(0)
	ds_read_b32 v4, v1
	s_add_i32 s0, 0, 0x20164
	v_mov_b32_e32 v1, s0
	ds_read_b32 v2, v1
	s_waitcnt lgkmcnt(1)
	v_cmp_ne_u32_e32 vcc, 0, v4
	s_cbranch_vccnz .LBB0_4031
	s_load_dwordx2 s[0:1], s[2:3], 0x4
	s_add_u32 s2, s34, 0x1000
	s_addc_u32 s3, s35, 0
	s_add_u32 s4, s34, 0x1100
	s_addc_u32 s5, s35, 0
	s_add_u32 s6, s34, 0x1200
	s_addc_u32 s7, s35, 0
	s_add_u32 s8, s34, 0x1300
	s_waitcnt lgkmcnt(0)
	s_mul_i32 s18, s0, s26
	s_addc_u32 s9, s35, 0
	s_mul_i32 s18, s18, s1
	s_mov_b32 s19, 1
	s_mov_b64 s[0:1], 0
	v_mov_b64_e32 v[2:3], s[34:35]
	v_mov_b64_e32 v[4:5], s[2:3]
	v_mov_b64_e32 v[6:7], s[4:5]
	v_mov_b64_e32 v[8:9], s[6:7]
	v_mov_b64_e32 v[10:11], s[8:9]
	s_branch .LBB0_4021

; __device__ __forceinline__ void xcd_barrier(const XcdBarrier& b) {
;     asm volatile("s_waitcnt vmcnt(0)" ::: "memory");
;     __syncthreads();
;     if (threadIdx.x == 0) {
;         unsigned* bar = b.bar;
;         __builtin_amdgcn_s_waitcnt(0);
;         unsigned nloc = b.st[0], nx = b.st[1];
;         if (nloc == 0u) { xcd_barrier_complete(bar, b.x, nloc, nx); b.st[0] = nloc; b.st[1] = nx; }
.LBB0_4862:
	v_readlane_b32 s0, v247, 8
	s_cmp_lt_i32 s0, 52
	s_branch .LBB0_4908
	v_readlane_b32 s0, v247, 2
	v_readlane_b32 s1, v247, 3
	s_waitcnt vmcnt(0)
	s_waitcnt vmcnt(0)
	v_writelane_b32 v247, s0, 2
	s_barrier
	s_nop 0
	v_writelane_b32 v247, s1, 3
	s_mov_b64 s[30:31], exec
	v_readlane_b32 s0, v247, 5
	v_readlane_b32 s1, v247, 6
	s_and_b64 s[0:1], s[30:31], s[0:1]
	s_mov_b64 exec, s[0:1]
	s_cbranch_execz .LBB0_4907
	s_add_i32 s0, 0, 0x20160
	v_mov_b32_e32 v0, s0
	s_waitcnt vmcnt(0) expcnt(0) lgkmcnt(0)
	ds_read_b32 v2, v0
	s_add_i32 s0, 0, 0x20164
	v_mov_b32_e32 v0, s0
	ds_read_b32 v0, v0
	s_waitcnt lgkmcnt(1)
	v_cmp_ne_u32_e32 vcc, 0, v2
	s_cbranch_vccnz .LBB0_4878
	v_readlane_b32 s10, v247, 2
	v_readlane_b32 s11, v247, 3
	s_add_u32 s2, s10, 0x1000
	s_addc_u32 s3, s11, 0
	s_load_dwordx2 s[0:1], s[4:5], 0x4
	s_add_u32 s4, s10, 0x1100
	s_addc_u32 s5, s11, 0
	s_add_u32 s6, s10, 0x1200
	s_addc_u32 s7, s11, 0
	s_add_u32 s8, s10, 0x1300
	s_waitcnt lgkmcnt(0)
	s_mul_i32 s18, s0, s19
	s_addc_u32 s9, s11, 0
	s_mul_i32 s18, s18, s1
	s_mov_b32 s19, 1
	s_mov_b64 s[0:1], 0
	v_mov_b64_e32 v[0:1], s[10:11]
	v_mov_b64_e32 v[2:3], s[2:3]
	v_mov_b64_e32 v[4:5], s[4:5]
	v_mov_b64_e32 v[6:7], s[6:7]
	v_mov_b64_e32 v[8:9], s[8:9]
	s_branch .LBB0_4868
